# c12
# speedup vs baseline: 1.0024x; 1.0024x over previous
.LBB2_2:
	s_lshl_b32 s0, s41, 15
	s_add_i32 s0, s42, s0
	s_add_i32 s41, s0, 0x2000
	s_lshl_b32 s0, s43, 15
	v_bfe_u32 v3, v0, 4, 1
	s_add_i32 s0, s51, s0
	s_add_i32 s42, s0, 0x2000
	v_and_b32_e32 v8, 15, v0
	v_lshlrev_b32_e32 v10, 8, v3
	v_lshlrev_b32_e32 v3, 9, v3
	s_and_b32 s0, s33, 0xc0
	v_lshrrev_b32_e32 v1, 5, v1
	v_or3_b32 v3, s0, v3, v8
	v_lshlrev_b32_e32 v9, 15, v1
	v_lshl_add_u32 v11, s29, 7, v10
	v_mul_u32_u24_e32 v3, 24, v3
	s_waitcnt vmcnt(5)
	v_or_b32_e32 v11, v11, v8
	v_or3_b32 v8, v10, s0, v8
	v_or_b32_e32 v3, v3, v9
	s_add_i32 s43, 0, 0x10000
	s_addk_i32 s52, 0x2000
	v_lshl_add_u32 v11, v11, 4, v9
	v_lshlrev_b32_e32 v1, 10, v1
	v_lshlrev_b32_e32 v8, 1, v8
	v_add_u32_e32 v9, s43, v3
	s_barrier
	s_barrier
	s_add_u32 s72, s4, s24
	s_addc_u32 s73, s5, s25
	s_add_u32 s72, s72, s28
	s_addc_u32 s73, s73, 0
	s_add_u32 s72, s72, 0x8000
	s_addc_u32 s73, s73, 0
	s_add_u32 s74, s72, 0x4000
	s_addc_u32 s75, s73, 0
	s_add_u32 s76, s6, s26
	s_addc_u32 s77, s7, s27
	s_add_u32 s76, s76, 0xc000
	s_addc_u32 s77, s77, 0
	s_add_u32 s78, s76, 0xc000
	s_addc_u32 s79, s77, 0
	s_add_u32 s80, s16, s3
	s_addc_u32 s81, s17, 0
	s_add_u32 s80, s80, 0x800
	s_addc_u32 s81, s81, 0
	s_add_i32 s0, s40, s39
	s_add_i32 s0, s0, s28
	s_mulk_i32 s38, 0x1800
	s_sub_i32 s0, s0, s38
	s_addk_i32 s0, 0x4000
	v_lshl_add_u64 v[6:7], s[26:27], 0, v[6:7]
	s_ashr_i32 s1, s0, 31
	v_lshl_add_u64 v[142:143], v[6:7], 0, s[0:1]
	s_add_i32 s0, s37, s36
	s_add_i32 s0, s0, s28
	s_mulk_i32 s35, 0x1800
	s_sub_i32 s0, s0, s35
	s_addk_i32 s0, 0x2000
	s_ashr_i32 s1, s0, 31
	v_lshl_add_u64 v[144:145], v[6:7], 0, s[0:1]
	s_add_i32 s0, s34, s31
	s_add_i32 s0, s0, s28
	s_mulk_i32 s30, 0x1800
	s_sub_i32 s0, s0, s30
	s_ashr_i32 s1, s0, 31
	v_lshl_add_u64 v[146:147], v[6:7], 0, s[0:1]
	s_add_u32 s0, s4, s24
	s_addc_u32 s1, s5, s25
	v_lshl_add_u64 v[4:5], s[0:1], 0, v[4:5]
	s_mov_b64 s[0:1], 0xa000
	v_add_u32_e32 v3, 0, v3
	v_add3_u32 v161, 0, v8, v1
	v_lshl_add_u64 v[148:149], v[4:5], 0, s[0:1]
	s_movk_i32 s0, 0xa000
	s_movk_i32 s4, 0xc000
	s_add_i32 s59, s43, s52
	s_add_i32 s58, s43, s41
	s_add_i32 s57, s43, s42
	s_movk_i32 s30, 0xe000
	v_add_u32_e32 v171, 0x2000, v3
	v_add_u32_e32 v167, 0x3800, v3
	v_add_u32_e32 v162, 0x2000, v9
	v_add_u32_e32 v1, 0x3800, v9
	v_add_u32_e32 v174, 0x2180, v3
	v_add_u32_e32 v173, 0x2300, v3
	v_add_u32_e32 v172, 0x2480, v3
	v_add_u32_e32 v170, 0x3980, v3
	v_add_u32_e32 v169, 0x3b00, v3
	v_add_u32_e32 v168, 0x3c80, v3
	v_add_u32_e32 v165, 0x2180, v9
	v_add_u32_e32 v164, 0x2300, v9
	v_add_u32_e32 v163, 0x2480, v9
	v_add_u32_e32 v160, 0x3980, v9
	v_add_u32_e32 v159, 0x3b00, v9
	v_add_u32_e32 v158, 0x3c80, v9
	s_mov_b32 s61, -2
	s_movk_i32 s62, 0x1000
	v_add_u32_e32 v175, 0, v11
	s_mov_b32 s1, -1
	s_add_i32 s63, s43, s28
	s_mov_b32 s5, -1
	s_add_i32 s60, s15, 0x18000
	s_mov_b64 s[24:25], 0xc000
	s_mov_b64 s[26:27], 0xc00800
	s_mov_b64 s[28:29], 0xd800
	s_add_i32 s54, s59, 0x1800
	s_add_i32 s52, s58, 0x1800
	s_add_i32 s51, s57, 0x1800
	v_add_u32_e32 v166, s43, v11
	s_mov_b32 s31, -1
	s_mov_b64 s[34:35], 0x18000
	s_mov_b64 s[36:37], 0xc01000
	s_mov_b64 s[38:39], 0x19800
	s_mov_b64 s[40:41], 0x1000
	s_mov_b64 s[42:43], 0x8000
	v_mov_b32_e32 v3, v2
	v_mov_b32_e32 v4, v2
	v_mov_b32_e32 v5, v2
	v_mov_b32_e32 v10, v2
	v_mov_b32_e32 v11, v2
	v_mov_b32_e32 v12, v2
	v_mov_b32_e32 v13, v2
	v_mov_b32_e32 v22, v2
	v_mov_b32_e32 v23, v2
	v_mov_b32_e32 v24, v2
	v_mov_b32_e32 v25, v2
	v_mov_b32_e32 v38, v2
	v_mov_b32_e32 v39, v2
	v_mov_b32_e32 v40, v2
	v_mov_b32_e32 v41, v2
	v_mov_b32_e32 v6, v2
	v_mov_b32_e32 v7, v2
	v_mov_b32_e32 v8, v2
	v_mov_b32_e32 v9, v2
	v_mov_b32_e32 v18, v2
	v_mov_b32_e32 v19, v2
	v_mov_b32_e32 v20, v2
	v_mov_b32_e32 v21, v2
	v_mov_b32_e32 v34, v2
	v_mov_b32_e32 v35, v2
	v_mov_b32_e32 v36, v2
	v_mov_b32_e32 v37, v2
	v_mov_b32_e32 v54, v2
	v_mov_b32_e32 v55, v2
	v_mov_b32_e32 v56, v2
	v_mov_b32_e32 v57, v2
	v_mov_b32_e32 v14, v2
	v_mov_b32_e32 v15, v2
	v_mov_b32_e32 v16, v2
	v_mov_b32_e32 v17, v2
	v_mov_b32_e32 v30, v2
	v_mov_b32_e32 v31, v2
	v_mov_b32_e32 v32, v2
	v_mov_b32_e32 v33, v2
	v_mov_b32_e32 v50, v2
	v_mov_b32_e32 v51, v2
	v_mov_b32_e32 v52, v2
	v_mov_b32_e32 v53, v2
	v_mov_b32_e32 v70, v2
	v_mov_b32_e32 v71, v2
	v_mov_b32_e32 v72, v2
	v_mov_b32_e32 v73, v2
	v_mov_b32_e32 v26, v2
	v_mov_b32_e32 v27, v2
	v_mov_b32_e32 v28, v2
	v_mov_b32_e32 v29, v2
	v_mov_b32_e32 v46, v2
	v_mov_b32_e32 v47, v2
	v_mov_b32_e32 v48, v2
	v_mov_b32_e32 v49, v2
	v_mov_b32_e32 v66, v2
	v_mov_b32_e32 v67, v2
	v_mov_b32_e32 v68, v2
	v_mov_b32_e32 v69, v2
	v_mov_b32_e32 v86, v2
	v_mov_b32_e32 v87, v2
	v_mov_b32_e32 v88, v2
	v_mov_b32_e32 v89, v2
	v_mov_b32_e32 v42, v2
	v_mov_b32_e32 v43, v2
	v_mov_b32_e32 v44, v2
	v_mov_b32_e32 v45, v2
	v_mov_b32_e32 v62, v2
	v_mov_b32_e32 v63, v2
	v_mov_b32_e32 v64, v2
	v_mov_b32_e32 v65, v2
	v_mov_b32_e32 v82, v2
	v_mov_b32_e32 v83, v2
	v_mov_b32_e32 v84, v2
	v_mov_b32_e32 v85, v2
	v_mov_b32_e32 v102, v2
	v_mov_b32_e32 v103, v2
	v_mov_b32_e32 v104, v2
	v_mov_b32_e32 v105, v2
	v_mov_b32_e32 v58, v2
	v_mov_b32_e32 v59, v2
	v_mov_b32_e32 v60, v2
	v_mov_b32_e32 v61, v2
	v_mov_b32_e32 v78, v2
	v_mov_b32_e32 v79, v2
	v_mov_b32_e32 v80, v2
	v_mov_b32_e32 v81, v2
	v_mov_b32_e32 v98, v2
	v_mov_b32_e32 v99, v2
	v_mov_b32_e32 v100, v2
	v_mov_b32_e32 v101, v2
	v_mov_b32_e32 v114, v2
	v_mov_b32_e32 v115, v2
	v_mov_b32_e32 v116, v2
	v_mov_b32_e32 v117, v2
	v_mov_b32_e32 v74, v2
	v_mov_b32_e32 v75, v2
	v_mov_b32_e32 v76, v2
	v_mov_b32_e32 v77, v2
	v_mov_b32_e32 v94, v2
	v_mov_b32_e32 v95, v2
	v_mov_b32_e32 v96, v2
	v_mov_b32_e32 v97, v2
	v_mov_b32_e32 v110, v2
	v_mov_b32_e32 v111, v2
	v_mov_b32_e32 v112, v2
	v_mov_b32_e32 v113, v2
	v_mov_b32_e32 v122, v2
	v_mov_b32_e32 v123, v2
	v_mov_b32_e32 v124, v2
	v_mov_b32_e32 v125, v2
	v_mov_b32_e32 v90, v2
	v_mov_b32_e32 v91, v2
	v_mov_b32_e32 v92, v2
	v_mov_b32_e32 v93, v2
	v_mov_b32_e32 v106, v2
	v_mov_b32_e32 v107, v2
	v_mov_b32_e32 v108, v2
	v_mov_b32_e32 v109, v2
	v_mov_b32_e32 v118, v2
	v_mov_b32_e32 v119, v2
	v_mov_b32_e32 v120, v2
	v_mov_b32_e32 v121, v2
	v_mov_b32_e32 v126, v2
	v_mov_b32_e32 v127, v2
	v_mov_b32_e32 v128, v2
	v_mov_b32_e32 v129, v2
	v_add_u32_e32 v176, 0x20000, v161
	v_mov_b32_e32 v177, 0x7f7f7f7f
	v_lshl_add_u64 v[150:151], s[44:45], 0, v[130:131]
	v_and_b32_e32 v142, 63, v0
	v_lshlrev_b32_e32 v150, 2, v142
	v_lshlrev_b32_e32 v142, 4, v142
	v_add_u32_e32 v143, 0x2000, v142
	v_add_u32_e32 v144, s18, v142
	v_add_u32_e32 v145, s20, v142
	v_add_u32_e32 v146, s22, v142
	v_add_u32_e32 v147, 0x1800, v144
	v_add_u32_e32 v148, 0x1800, v145
	v_add_u32_e32 v149, 0x1800, v146
	v_add_u32_e32 v151, 0x800, v150
	s_add_i32 s44, s62, 0xfffff000
	s_and_b32 s44, s44, 0x1000
.LBB2_3:
	ds_read_b128 v[202:205], v175
	ds_read_b128 v[206:209], v175 offset:256
	ds_read_b128 v[210:213], v175 offset:512
	ds_read_b128 v[214:217], v175 offset:768
	ds_read_b128 v[218:221], v175 offset:1024
	ds_read_b128 v[222:225], v175 offset:1280
	ds_read_b128 v[226:229], v175 offset:1536
	ds_read_b128 v[230:233], v175 offset:1792
	ds_read2_b64 v[178:181], v171 offset1:1
	ds_read2_b64 v[182:185], v171 offset0:2 offset1:48
	ds_read2_b64 v[186:189], v171 offset0:49 offset1:50
	s_mov_b32 m0, s59
	ds_read2_b64 v[190:193], v171 offset0:96 offset1:97
	global_load_lds_dwordx4 v144, s[76:77]
	s_mov_b32 m0, s58
	ds_read2_b64 v[194:197], v171 offset0:98 offset1:144
	global_load_lds_dwordx4 v145, s[76:77]
	s_mov_b32 m0, s57
	ds_read2_b64 v[198:201], v171 offset0:145 offset1:146
	global_load_lds_dwordx4 v146, s[76:77]
	v_add_u32_e32 v152, s44, v176
	ds_read_u16 v240, v152
	ds_read_u16 v241, v152 offset:32
	ds_read_u16 v242, v152 offset:64
	s_add_i32 s44, s62, 0xfffff800
	s_and_b32 s44, s44, 0x1800
	s_add_i32 m0, s50, s44
	ds_read_u16 v243, v152 offset:96
	global_load_lds_dword v150, s[80:81]
	s_waitcnt vmcnt(6)
	s_waitcnt lgkmcnt(0)
	s_barrier
	v_mfma_scale_f32_16x16x128_f8f6f4 v[126:129], v[202:205], v[178:183], v[126:129], v177, v240 op_sel_hi:[0,0,0] cbsz:4 blgp:2
	v_mfma_scale_f32_16x16x128_f8f6f4 v[122:125], v[206:209], v[178:183], v[122:125], v177, v240 op_sel_hi:[0,0,0] cbsz:4 blgp:2
	v_mfma_scale_f32_16x16x128_f8f6f4 v[114:117], v[210:213], v[178:183], v[114:117], v177, v240 op_sel_hi:[0,0,0] cbsz:4 blgp:2
	v_mfma_scale_f32_16x16x128_f8f6f4 v[102:105], v[214:217], v[178:183], v[102:105], v177, v240 op_sel_hi:[0,0,0] cbsz:4 blgp:2
	v_mfma_scale_f32_16x16x128_f8f6f4 v[86:89], v[218:221], v[178:183], v[86:89], v177, v240 op_sel_hi:[0,0,0] cbsz:4 blgp:2
	v_mfma_scale_f32_16x16x128_f8f6f4 v[70:73], v[222:225], v[178:183], v[70:73], v177, v240 op_sel_hi:[0,0,0] cbsz:4 blgp:2
	v_mfma_scale_f32_16x16x128_f8f6f4 v[54:57], v[226:229], v[178:183], v[54:57], v177, v240 op_sel_hi:[0,0,0] cbsz:4 blgp:2
	v_mfma_scale_f32_16x16x128_f8f6f4 v[38:41], v[230:233], v[178:183], v[38:41], v177, v240 op_sel_hi:[0,0,0] cbsz:4 blgp:2
	v_mfma_scale_f32_16x16x128_f8f6f4 v[118:121], v[202:205], v[184:189], v[118:121], v177, v241 op_sel_hi:[0,0,0] cbsz:4 blgp:2
	v_mfma_scale_f32_16x16x128_f8f6f4 v[110:113], v[206:209], v[184:189], v[110:113], v177, v241 op_sel_hi:[0,0,0] cbsz:4 blgp:2
	v_mfma_scale_f32_16x16x128_f8f6f4 v[98:101], v[210:213], v[184:189], v[98:101], v177, v241 op_sel_hi:[0,0,0] cbsz:4 blgp:2
	v_mfma_scale_f32_16x16x128_f8f6f4 v[82:85], v[214:217], v[184:189], v[82:85], v177, v241 op_sel_hi:[0,0,0] cbsz:4 blgp:2
	v_mfma_scale_f32_16x16x128_f8f6f4 v[66:69], v[218:221], v[184:189], v[66:69], v177, v241 op_sel_hi:[0,0,0] cbsz:4 blgp:2
	v_mfma_scale_f32_16x16x128_f8f6f4 v[50:53], v[222:225], v[184:189], v[50:53], v177, v241 op_sel_hi:[0,0,0] cbsz:4 blgp:2
	v_mfma_scale_f32_16x16x128_f8f6f4 v[34:37], v[226:229], v[184:189], v[34:37], v177, v241 op_sel_hi:[0,0,0] cbsz:4 blgp:2
	v_mfma_scale_f32_16x16x128_f8f6f4 v[106:109], v[202:205], v[190:195], v[106:109], v177, v242 op_sel_hi:[0,0,0] cbsz:4 blgp:2
	v_mfma_scale_f32_16x16x128_f8f6f4 v[94:97], v[206:209], v[190:195], v[94:97], v177, v242 op_sel_hi:[0,0,0] cbsz:4 blgp:2
	v_mfma_scale_f32_16x16x128_f8f6f4 v[78:81], v[210:213], v[190:195], v[78:81], v177, v242 op_sel_hi:[0,0,0] cbsz:4 blgp:2
	v_mfma_scale_f32_16x16x128_f8f6f4 v[62:65], v[214:217], v[190:195], v[62:65], v177, v242 op_sel_hi:[0,0,0] cbsz:4 blgp:2
	v_mfma_scale_f32_16x16x128_f8f6f4 v[46:49], v[218:221], v[190:195], v[46:49], v177, v242 op_sel_hi:[0,0,0] cbsz:4 blgp:2
	v_mfma_scale_f32_16x16x128_f8f6f4 v[30:33], v[222:225], v[190:195], v[30:33], v177, v242 op_sel_hi:[0,0,0] cbsz:4 blgp:2
	v_mfma_scale_f32_16x16x128_f8f6f4 v[90:93], v[202:205], v[196:201], v[90:93], v177, v243 op_sel_hi:[0,0,0] cbsz:4 blgp:2
	v_mfma_scale_f32_16x16x128_f8f6f4 v[74:77], v[206:209], v[196:201], v[74:77], v177, v243 op_sel_hi:[0,0,0] cbsz:4 blgp:2
	v_mfma_scale_f32_16x16x128_f8f6f4 v[58:61], v[210:213], v[196:201], v[58:61], v177, v243 op_sel_hi:[0,0,0] cbsz:4 blgp:2
	v_mfma_scale_f32_16x16x128_f8f6f4 v[42:45], v[214:217], v[196:201], v[42:45], v177, v243 op_sel_hi:[0,0,0] cbsz:4 blgp:2
	v_mfma_scale_f32_16x16x128_f8f6f4 v[26:29], v[218:221], v[196:201], v[26:29], v177, v243 op_sel_hi:[0,0,0] cbsz:4 blgp:2
	v_mfma_scale_f32_16x16x128_f8f6f4 v[178:181], v[230:233], v[184:189], v[22:25], v177, v241 op_sel_hi:[0,0,0] cbsz:4 blgp:2
	v_mfma_scale_f32_16x16x128_f8f6f4 v[182:185], v[226:229], v[190:195], v[18:21], v177, v242 op_sel_hi:[0,0,0] cbsz:4 blgp:2
	v_mfma_scale_f32_16x16x128_f8f6f4 v[186:189], v[230:233], v[190:195], v[10:13], v177, v242 op_sel_hi:[0,0,0] cbsz:4 blgp:2
	v_mfma_scale_f32_16x16x128_f8f6f4 v[190:193], v[222:225], v[196:201], v[14:17], v177, v243 op_sel_hi:[0,0,0] cbsz:4 blgp:2
	v_mfma_scale_f32_16x16x128_f8f6f4 v[234:237], v[226:229], v[196:201], v[6:9], v177, v243 op_sel_hi:[0,0,0] cbsz:4 blgp:2
	v_mfma_scale_f32_16x16x128_f8f6f4 v[194:197], v[230:233], v[196:201], v[2:5], v177, v243 op_sel_hi:[0,0,0] cbsz:4 blgp:2
	s_barrier
	ds_read2_b64 v[2:5], v167 offset1:1
	s_mov_b32 m0, s54
	ds_read2_b64 v[6:9], v167 offset0:2 offset1:48
	global_load_lds_dwordx4 v147, s[76:77]
	s_mov_b32 m0, s52
	ds_read2_b64 v[10:13], v167 offset0:49 offset1:50
	global_load_lds_dwordx4 v148, s[76:77]
	s_mov_b32 m0, s51
	ds_read2_b64 v[14:17], v167 offset0:96 offset1:97
	global_load_lds_dwordx4 v149, s[76:77]
	s_mov_b32 m0, s15
	ds_read2_b64 v[18:21], v167 offset0:98 offset1:144
	global_load_lds_dwordx4 v142, s[72:73]
	s_mov_b32 m0, s46
	ds_read2_b64 v[22:25], v167 offset0:145 offset1:146
	global_load_lds_dwordx4 v143, s[72:73]
	s_waitcnt vmcnt(5)
	s_waitcnt lgkmcnt(0)
	s_barrier
	v_mfma_scale_f32_16x16x128_f8f6f4 v[126:129], v[202:205], v[2:7], v[126:129], v177, v240 op_sel:[0,1,0] op_sel_hi:[0,0,0] cbsz:4 blgp:2
	v_mfma_scale_f32_16x16x128_f8f6f4 v[122:125], v[206:209], v[2:7], v[122:125], v177, v240 op_sel:[0,1,0] op_sel_hi:[0,0,0] cbsz:4 blgp:2
	v_mfma_scale_f32_16x16x128_f8f6f4 v[114:117], v[210:213], v[2:7], v[114:117], v177, v240 op_sel:[0,1,0] op_sel_hi:[0,0,0] cbsz:4 blgp:2
	v_mfma_scale_f32_16x16x128_f8f6f4 v[102:105], v[214:217], v[2:7], v[102:105], v177, v240 op_sel:[0,1,0] op_sel_hi:[0,0,0] cbsz:4 blgp:2
	v_mfma_scale_f32_16x16x128_f8f6f4 v[86:89], v[218:221], v[2:7], v[86:89], v177, v240 op_sel:[0,1,0] op_sel_hi:[0,0,0] cbsz:4 blgp:2
	v_mfma_scale_f32_16x16x128_f8f6f4 v[70:73], v[222:225], v[2:7], v[70:73], v177, v240 op_sel:[0,1,0] op_sel_hi:[0,0,0] cbsz:4 blgp:2
	v_mfma_scale_f32_16x16x128_f8f6f4 v[54:57], v[226:229], v[2:7], v[54:57], v177, v240 op_sel:[0,1,0] op_sel_hi:[0,0,0] cbsz:4 blgp:2
	v_mfma_scale_f32_16x16x128_f8f6f4 v[38:41], v[230:233], v[2:7], v[38:41], v177, v240 op_sel:[0,1,0] op_sel_hi:[0,0,0] cbsz:4 blgp:2
	v_mfma_scale_f32_16x16x128_f8f6f4 v[118:121], v[202:205], v[8:13], v[118:121], v177, v241 op_sel:[0,1,0] op_sel_hi:[0,0,0] cbsz:4 blgp:2
	v_mfma_scale_f32_16x16x128_f8f6f4 v[110:113], v[206:209], v[8:13], v[110:113], v177, v241 op_sel:[0,1,0] op_sel_hi:[0,0,0] cbsz:4 blgp:2
	v_mfma_scale_f32_16x16x128_f8f6f4 v[98:101], v[210:213], v[8:13], v[98:101], v177, v241 op_sel:[0,1,0] op_sel_hi:[0,0,0] cbsz:4 blgp:2
	v_mfma_scale_f32_16x16x128_f8f6f4 v[82:85], v[214:217], v[8:13], v[82:85], v177, v241 op_sel:[0,1,0] op_sel_hi:[0,0,0] cbsz:4 blgp:2
	v_mfma_scale_f32_16x16x128_f8f6f4 v[66:69], v[218:221], v[8:13], v[66:69], v177, v241 op_sel:[0,1,0] op_sel_hi:[0,0,0] cbsz:4 blgp:2
	v_mfma_scale_f32_16x16x128_f8f6f4 v[50:53], v[222:225], v[8:13], v[50:53], v177, v241 op_sel:[0,1,0] op_sel_hi:[0,0,0] cbsz:4 blgp:2
	v_mfma_scale_f32_16x16x128_f8f6f4 v[34:37], v[226:229], v[8:13], v[34:37], v177, v241 op_sel:[0,1,0] op_sel_hi:[0,0,0] cbsz:4 blgp:2
	v_mfma_scale_f32_16x16x128_f8f6f4 v[106:109], v[202:205], v[14:19], v[106:109], v177, v242 op_sel:[0,1,0] op_sel_hi:[0,0,0] cbsz:4 blgp:2
	v_mfma_scale_f32_16x16x128_f8f6f4 v[94:97], v[206:209], v[14:19], v[94:97], v177, v242 op_sel:[0,1,0] op_sel_hi:[0,0,0] cbsz:4 blgp:2
	v_mfma_scale_f32_16x16x128_f8f6f4 v[78:81], v[210:213], v[14:19], v[78:81], v177, v242 op_sel:[0,1,0] op_sel_hi:[0,0,0] cbsz:4 blgp:2
	v_mfma_scale_f32_16x16x128_f8f6f4 v[62:65], v[214:217], v[14:19], v[62:65], v177, v242 op_sel:[0,1,0] op_sel_hi:[0,0,0] cbsz:4 blgp:2
	v_mfma_scale_f32_16x16x128_f8f6f4 v[46:49], v[218:221], v[14:19], v[46:49], v177, v242 op_sel:[0,1,0] op_sel_hi:[0,0,0] cbsz:4 blgp:2
	v_mfma_scale_f32_16x16x128_f8f6f4 v[30:33], v[222:225], v[14:19], v[30:33], v177, v242 op_sel:[0,1,0] op_sel_hi:[0,0,0] cbsz:4 blgp:2
	v_mfma_scale_f32_16x16x128_f8f6f4 v[90:93], v[202:205], v[20:25], v[90:93], v177, v243 op_sel:[0,1,0] op_sel_hi:[0,0,0] cbsz:4 blgp:2
	v_mfma_scale_f32_16x16x128_f8f6f4 v[74:77], v[206:209], v[20:25], v[74:77], v177, v243 op_sel:[0,1,0] op_sel_hi:[0,0,0] cbsz:4 blgp:2
	v_mfma_scale_f32_16x16x128_f8f6f4 v[58:61], v[210:213], v[20:25], v[58:61], v177, v243 op_sel:[0,1,0] op_sel_hi:[0,0,0] cbsz:4 blgp:2
	v_mfma_scale_f32_16x16x128_f8f6f4 v[42:45], v[214:217], v[20:25], v[42:45], v177, v243 op_sel:[0,1,0] op_sel_hi:[0,0,0] cbsz:4 blgp:2
	v_mfma_scale_f32_16x16x128_f8f6f4 v[26:29], v[218:221], v[20:25], v[26:29], v177, v243 op_sel:[0,1,0] op_sel_hi:[0,0,0] cbsz:4 blgp:2
	v_mfma_scale_f32_16x16x128_f8f6f4 v[178:181], v[230:233], v[8:13], v[178:181], v177, v241 op_sel:[0,1,0] op_sel_hi:[0,0,0] cbsz:4 blgp:2
	v_mfma_scale_f32_16x16x128_f8f6f4 v[182:185], v[226:229], v[14:19], v[182:185], v177, v242 op_sel:[0,1,0] op_sel_hi:[0,0,0] cbsz:4 blgp:2
	v_mfma_scale_f32_16x16x128_f8f6f4 v[186:189], v[230:233], v[14:19], v[186:189], v177, v242 op_sel:[0,1,0] op_sel_hi:[0,0,0] cbsz:4 blgp:2
	v_mfma_scale_f32_16x16x128_f8f6f4 v[190:193], v[222:225], v[20:25], v[190:193], v177, v243 op_sel:[0,1,0] op_sel_hi:[0,0,0] cbsz:4 blgp:2
	v_mfma_scale_f32_16x16x128_f8f6f4 v[198:201], v[226:229], v[20:25], v[234:237], v177, v243 op_sel:[0,1,0] op_sel_hi:[0,0,0] cbsz:4 blgp:2
	v_mfma_scale_f32_16x16x128_f8f6f4 v[194:197], v[230:233], v[20:25], v[194:197], v177, v243 op_sel:[0,1,0] op_sel_hi:[0,0,0] cbsz:4 blgp:2
	s_barrier
	ds_read_b128 v[202:205], v166
	ds_read_b128 v[206:209], v166 offset:256
	ds_read_b128 v[210:213], v166 offset:512
	ds_read_b128 v[214:217], v166 offset:768
	ds_read_b128 v[218:221], v166 offset:1024
	ds_read_b128 v[222:225], v166 offset:1280
	ds_read_b128 v[226:229], v166 offset:1536
	ds_read_b128 v[230:233], v166 offset:1792
	ds_read2_b64 v[2:5], v162 offset1:1
	ds_read2_b64 v[6:9], v162 offset0:2 offset1:48
	ds_read2_b64 v[10:13], v162 offset0:49 offset1:50
	s_mov_b32 m0, s47
	ds_read2_b64 v[14:17], v162 offset0:96 offset1:97
	global_load_lds_dwordx4 v144, s[78:79]
	s_mov_b32 m0, s48
	ds_read2_b64 v[18:21], v162 offset0:98 offset1:144
	global_load_lds_dwordx4 v145, s[78:79]
	s_mov_b32 m0, s49
	ds_read2_b64 v[22:25], v162 offset0:145 offset1:146
	global_load_lds_dwordx4 v146, s[78:79]
	v_add_u32_e32 v234, s44, v176
	ds_read_u16 v242, v234
	ds_read_u16 v243, v234 offset:32
	ds_read_u16 v244, v234 offset:64
	s_and_b32 s44, s62, 0x1000
	s_add_i32 m0, s50, s44
	ds_read_u16 v245, v234 offset:96
	global_load_lds_dword v151, s[80:81]
	s_waitcnt vmcnt(6)
	s_waitcnt lgkmcnt(0)
	s_barrier
	v_mfma_scale_f32_16x16x128_f8f6f4 v[126:129], v[202:205], v[2:7], v[126:129], v177, v242 op_sel_hi:[0,0,0] cbsz:4 blgp:2
	v_mfma_scale_f32_16x16x128_f8f6f4 v[122:125], v[206:209], v[2:7], v[122:125], v177, v242 op_sel_hi:[0,0,0] cbsz:4 blgp:2
	v_mfma_scale_f32_16x16x128_f8f6f4 v[114:117], v[210:213], v[2:7], v[114:117], v177, v242 op_sel_hi:[0,0,0] cbsz:4 blgp:2
	v_mfma_scale_f32_16x16x128_f8f6f4 v[102:105], v[214:217], v[2:7], v[102:105], v177, v242 op_sel_hi:[0,0,0] cbsz:4 blgp:2
	v_mfma_scale_f32_16x16x128_f8f6f4 v[86:89], v[218:221], v[2:7], v[86:89], v177, v242 op_sel_hi:[0,0,0] cbsz:4 blgp:2
	v_mfma_scale_f32_16x16x128_f8f6f4 v[70:73], v[222:225], v[2:7], v[70:73], v177, v242 op_sel_hi:[0,0,0] cbsz:4 blgp:2
	v_mfma_scale_f32_16x16x128_f8f6f4 v[54:57], v[226:229], v[2:7], v[54:57], v177, v242 op_sel_hi:[0,0,0] cbsz:4 blgp:2
	v_mfma_scale_f32_16x16x128_f8f6f4 v[38:41], v[230:233], v[2:7], v[38:41], v177, v242 op_sel_hi:[0,0,0] cbsz:4 blgp:2
	v_mfma_scale_f32_16x16x128_f8f6f4 v[118:121], v[202:205], v[8:13], v[118:121], v177, v243 op_sel_hi:[0,0,0] cbsz:4 blgp:2
	v_mfma_scale_f32_16x16x128_f8f6f4 v[110:113], v[206:209], v[8:13], v[110:113], v177, v243 op_sel_hi:[0,0,0] cbsz:4 blgp:2
	v_mfma_scale_f32_16x16x128_f8f6f4 v[98:101], v[210:213], v[8:13], v[98:101], v177, v243 op_sel_hi:[0,0,0] cbsz:4 blgp:2
	v_mfma_scale_f32_16x16x128_f8f6f4 v[82:85], v[214:217], v[8:13], v[82:85], v177, v243 op_sel_hi:[0,0,0] cbsz:4 blgp:2
	v_mfma_scale_f32_16x16x128_f8f6f4 v[66:69], v[218:221], v[8:13], v[66:69], v177, v243 op_sel_hi:[0,0,0] cbsz:4 blgp:2
	v_mfma_scale_f32_16x16x128_f8f6f4 v[50:53], v[222:225], v[8:13], v[50:53], v177, v243 op_sel_hi:[0,0,0] cbsz:4 blgp:2
	v_mfma_scale_f32_16x16x128_f8f6f4 v[34:37], v[226:229], v[8:13], v[34:37], v177, v243 op_sel_hi:[0,0,0] cbsz:4 blgp:2
	v_mfma_scale_f32_16x16x128_f8f6f4 v[106:109], v[202:205], v[14:19], v[106:109], v177, v244 op_sel_hi:[0,0,0] cbsz:4 blgp:2
	v_mfma_scale_f32_16x16x128_f8f6f4 v[94:97], v[206:209], v[14:19], v[94:97], v177, v244 op_sel_hi:[0,0,0] cbsz:4 blgp:2
	v_mfma_scale_f32_16x16x128_f8f6f4 v[78:81], v[210:213], v[14:19], v[78:81], v177, v244 op_sel_hi:[0,0,0] cbsz:4 blgp:2
	v_mfma_scale_f32_16x16x128_f8f6f4 v[62:65], v[214:217], v[14:19], v[62:65], v177, v244 op_sel_hi:[0,0,0] cbsz:4 blgp:2
	v_mfma_scale_f32_16x16x128_f8f6f4 v[46:49], v[218:221], v[14:19], v[46:49], v177, v244 op_sel_hi:[0,0,0] cbsz:4 blgp:2
	v_mfma_scale_f32_16x16x128_f8f6f4 v[30:33], v[222:225], v[14:19], v[30:33], v177, v244 op_sel_hi:[0,0,0] cbsz:4 blgp:2
	v_mfma_scale_f32_16x16x128_f8f6f4 v[238:241], v[226:229], v[14:19], v[182:185], v177, v244 op_sel_hi:[0,0,0] cbsz:4 blgp:2
	v_mfma_scale_f32_16x16x128_f8f6f4 v[14:17], v[230:233], v[14:19], v[186:189], v177, v244 op_sel_hi:[0,0,0] cbsz:4 blgp:2
	v_mfma_scale_f32_16x16x128_f8f6f4 v[90:93], v[202:205], v[20:25], v[90:93], v177, v245 op_sel_hi:[0,0,0] cbsz:4 blgp:2
	v_mfma_scale_f32_16x16x128_f8f6f4 v[74:77], v[206:209], v[20:25], v[74:77], v177, v245 op_sel_hi:[0,0,0] cbsz:4 blgp:2
	v_mfma_scale_f32_16x16x128_f8f6f4 v[58:61], v[210:213], v[20:25], v[58:61], v177, v245 op_sel_hi:[0,0,0] cbsz:4 blgp:2
	v_mfma_scale_f32_16x16x128_f8f6f4 v[42:45], v[214:217], v[20:25], v[42:45], v177, v245 op_sel_hi:[0,0,0] cbsz:4 blgp:2
	v_mfma_scale_f32_16x16x128_f8f6f4 v[26:29], v[218:221], v[20:25], v[26:29], v177, v245 op_sel_hi:[0,0,0] cbsz:4 blgp:2
	v_mfma_scale_f32_16x16x128_f8f6f4 v[234:237], v[230:233], v[8:13], v[178:181], v177, v243 op_sel_hi:[0,0,0] cbsz:4 blgp:2
	v_mfma_scale_f32_16x16x128_f8f6f4 v[190:193], v[222:225], v[20:25], v[190:193], v177, v245 op_sel_hi:[0,0,0] cbsz:4 blgp:2
	v_mfma_scale_f32_16x16x128_f8f6f4 v[198:201], v[226:229], v[20:25], v[198:201], v177, v245 op_sel_hi:[0,0,0] cbsz:4 blgp:2
	v_mfma_scale_f32_16x16x128_f8f6f4 v[194:197], v[230:233], v[20:25], v[194:197], v177, v245 op_sel_hi:[0,0,0] cbsz:4 blgp:2
	s_barrier
	ds_read2_b64 v[2:5], v1 offset1:1
	s_mov_b32 m0, s53
	ds_read2_b64 v[6:9], v1 offset0:2 offset1:48
	global_load_lds_dwordx4 v147, s[78:79]
	s_mov_b32 m0, s55
	ds_read2_b64 v[10:13], v1 offset0:49 offset1:50
	global_load_lds_dwordx4 v148, s[78:79]
	s_mov_b32 m0, s56
	ds_read2_b64 v[178:181], v159 offset1:1
	global_load_lds_dwordx4 v149, s[78:79]
	s_mov_b32 m0, s63
	ds_read2_b64 v[182:185], v159 offset0:2 offset1:48
	global_load_lds_dwordx4 v142, s[74:75]
	s_mov_b32 m0, s60
	ds_read2_b64 v[186:189], v159 offset0:49 offset1:50
	global_load_lds_dwordx4 v143, s[74:75]
	s_waitcnt vmcnt(5)
	s_waitcnt lgkmcnt(0)
	s_barrier
	v_mfma_scale_f32_16x16x128_f8f6f4 v[126:129], v[202:205], v[2:7], v[126:129], v177, v242 op_sel:[0,1,0] op_sel_hi:[0,0,0] cbsz:4 blgp:2
	v_mfma_scale_f32_16x16x128_f8f6f4 v[122:125], v[206:209], v[2:7], v[122:125], v177, v242 op_sel:[0,1,0] op_sel_hi:[0,0,0] cbsz:4 blgp:2
	v_mfma_scale_f32_16x16x128_f8f6f4 v[114:117], v[210:213], v[2:7], v[114:117], v177, v242 op_sel:[0,1,0] op_sel_hi:[0,0,0] cbsz:4 blgp:2
	v_mfma_scale_f32_16x16x128_f8f6f4 v[102:105], v[214:217], v[2:7], v[102:105], v177, v242 op_sel:[0,1,0] op_sel_hi:[0,0,0] cbsz:4 blgp:2
	v_mfma_scale_f32_16x16x128_f8f6f4 v[86:89], v[218:221], v[2:7], v[86:89], v177, v242 op_sel:[0,1,0] op_sel_hi:[0,0,0] cbsz:4 blgp:2
	v_mfma_scale_f32_16x16x128_f8f6f4 v[70:73], v[222:225], v[2:7], v[70:73], v177, v242 op_sel:[0,1,0] op_sel_hi:[0,0,0] cbsz:4 blgp:2
	v_mfma_scale_f32_16x16x128_f8f6f4 v[54:57], v[226:229], v[2:7], v[54:57], v177, v242 op_sel:[0,1,0] op_sel_hi:[0,0,0] cbsz:4 blgp:2
	v_mfma_scale_f32_16x16x128_f8f6f4 v[38:41], v[230:233], v[2:7], v[38:41], v177, v242 op_sel:[0,1,0] op_sel_hi:[0,0,0] cbsz:4 blgp:2
	v_mfma_scale_f32_16x16x128_f8f6f4 v[118:121], v[202:205], v[8:13], v[118:121], v177, v243 op_sel:[0,1,0] op_sel_hi:[0,0,0] cbsz:4 blgp:2
	v_mfma_scale_f32_16x16x128_f8f6f4 v[110:113], v[206:209], v[8:13], v[110:113], v177, v243 op_sel:[0,1,0] op_sel_hi:[0,0,0] cbsz:4 blgp:2
	v_mfma_scale_f32_16x16x128_f8f6f4 v[98:101], v[210:213], v[8:13], v[98:101], v177, v243 op_sel:[0,1,0] op_sel_hi:[0,0,0] cbsz:4 blgp:2
	v_mfma_scale_f32_16x16x128_f8f6f4 v[82:85], v[214:217], v[8:13], v[82:85], v177, v243 op_sel:[0,1,0] op_sel_hi:[0,0,0] cbsz:4 blgp:2
	v_mfma_scale_f32_16x16x128_f8f6f4 v[66:69], v[218:221], v[8:13], v[66:69], v177, v243 op_sel:[0,1,0] op_sel_hi:[0,0,0] cbsz:4 blgp:2
	v_mfma_scale_f32_16x16x128_f8f6f4 v[50:53], v[222:225], v[8:13], v[50:53], v177, v243 op_sel:[0,1,0] op_sel_hi:[0,0,0] cbsz:4 blgp:2
	v_mfma_scale_f32_16x16x128_f8f6f4 v[34:37], v[226:229], v[8:13], v[34:37], v177, v243 op_sel:[0,1,0] op_sel_hi:[0,0,0] cbsz:4 blgp:2
	v_mfma_scale_f32_16x16x128_f8f6f4 v[22:25], v[230:233], v[8:13], v[234:237], v177, v243 op_sel:[0,1,0] op_sel_hi:[0,0,0] cbsz:4 blgp:2
	v_mfma_scale_f32_16x16x128_f8f6f4 v[106:109], v[202:205], v[178:183], v[106:109], v177, v244 op_sel:[0,1,0] op_sel_hi:[0,0,0] cbsz:4 blgp:2
	v_mfma_scale_f32_16x16x128_f8f6f4 v[94:97], v[206:209], v[178:183], v[94:97], v177, v244 op_sel:[0,1,0] op_sel_hi:[0,0,0] cbsz:4 blgp:2
	v_mfma_scale_f32_16x16x128_f8f6f4 v[78:81], v[210:213], v[178:183], v[78:81], v177, v244 op_sel:[0,1,0] op_sel_hi:[0,0,0] cbsz:4 blgp:2
	v_mfma_scale_f32_16x16x128_f8f6f4 v[62:65], v[214:217], v[178:183], v[62:65], v177, v244 op_sel:[0,1,0] op_sel_hi:[0,0,0] cbsz:4 blgp:2
	v_mfma_scale_f32_16x16x128_f8f6f4 v[46:49], v[218:221], v[178:183], v[46:49], v177, v244 op_sel:[0,1,0] op_sel_hi:[0,0,0] cbsz:4 blgp:2
	v_mfma_scale_f32_16x16x128_f8f6f4 v[30:33], v[222:225], v[178:183], v[30:33], v177, v244 op_sel:[0,1,0] op_sel_hi:[0,0,0] cbsz:4 blgp:2
	v_mfma_scale_f32_16x16x128_f8f6f4 v[18:21], v[226:229], v[178:183], v[238:241], v177, v244 op_sel:[0,1,0] op_sel_hi:[0,0,0] cbsz:4 blgp:2
	v_mfma_scale_f32_16x16x128_f8f6f4 v[10:13], v[230:233], v[178:183], v[14:17], v177, v244 op_sel:[0,1,0] op_sel_hi:[0,0,0] cbsz:4 blgp:2
	v_mfma_scale_f32_16x16x128_f8f6f4 v[90:93], v[202:205], v[184:189], v[90:93], v177, v245 op_sel:[0,1,0] op_sel_hi:[0,0,0] cbsz:4 blgp:2
	v_mfma_scale_f32_16x16x128_f8f6f4 v[74:77], v[206:209], v[184:189], v[74:77], v177, v245 op_sel:[0,1,0] op_sel_hi:[0,0,0] cbsz:4 blgp:2
	v_mfma_scale_f32_16x16x128_f8f6f4 v[58:61], v[210:213], v[184:189], v[58:61], v177, v245 op_sel:[0,1,0] op_sel_hi:[0,0,0] cbsz:4 blgp:2
	v_mfma_scale_f32_16x16x128_f8f6f4 v[42:45], v[214:217], v[184:189], v[42:45], v177, v245 op_sel:[0,1,0] op_sel_hi:[0,0,0] cbsz:4 blgp:2
	v_mfma_scale_f32_16x16x128_f8f6f4 v[26:29], v[218:221], v[184:189], v[26:29], v177, v245 op_sel:[0,1,0] op_sel_hi:[0,0,0] cbsz:4 blgp:2
	v_mfma_scale_f32_16x16x128_f8f6f4 v[14:17], v[222:225], v[184:189], v[190:193], v177, v245 op_sel:[0,1,0] op_sel_hi:[0,0,0] cbsz:4 blgp:2
	v_mfma_scale_f32_16x16x128_f8f6f4 v[6:9], v[226:229], v[184:189], v[198:201], v177, v245 op_sel:[0,1,0] op_sel_hi:[0,0,0] cbsz:4 blgp:2
	v_mfma_scale_f32_16x16x128_f8f6f4 v[2:5], v[230:233], v[184:189], v[194:197], v177, v245 op_sel:[0,1,0] op_sel_hi:[0,0,0] cbsz:4 blgp:2
	s_add_i32 s61, s61, 2
	s_addk_i32 s62, 0x1000
	s_add_u32 s72, s72, 0x8000
	s_addc_u32 s73, s73, 0
	s_add_u32 s74, s74, 0x8000
	s_addc_u32 s75, s75, 0
	s_add_u32 s76, s76, 0x18000
	s_addc_u32 s77, s77, 0
	s_add_u32 s78, s78, 0x18000
	s_addc_u32 s79, s79, 0
	s_add_u32 s80, s80, 0x1000
	s_addc_u32 s81, s81, 0
	s_add_i32 s44, s62, 0xfffff000
	s_and_b32 s44, s44, 0x1000
	s_cmp_lt_u32 s61, 4
	s_barrier
	s_cbranch_scc1 .LBB2_3
	ds_read_b128 v[154:157], v175
	ds_read_b128 v[186:189], v175 offset:256
	ds_read_b128 v[190:193], v175 offset:512
	ds_read_b128 v[194:197], v175 offset:768
	ds_read_b128 v[198:201], v175 offset:1024
	ds_read_b128 v[202:205], v175 offset:1280
	ds_read_b128 v[206:209], v175 offset:1536
	ds_read_b128 v[210:213], v175 offset:1792
	ds_read_b64 v[142:143], v171
	ds_read_b64 v[144:145], v171 offset:8
	ds_read_b64 v[146:147], v171 offset:16
	ds_read_b64 v[148:149], v174
	ds_read_b64 v[150:151], v174 offset:8
	ds_read_b64 v[152:153], v174 offset:16
	ds_read_b64 v[174:175], v173
	ds_read_b64 v[176:177], v173 offset:8
	ds_read_b64 v[178:179], v173 offset:16
	ds_read_b64 v[180:181], v172
	ds_read_b64 v[182:183], v172 offset:8
	ds_read_b64 v[184:185], v172 offset:16
	v_add_u32_e32 v171, 0x21000, v161
	v_add_u32_e32 v172, 0x21020, v161
	v_add_u32_e32 v173, 0x21040, v161
	v_add_u32_e32 v214, 0x21060, v161
	s_mov_b64 s[0:1], 0x1c000
	s_mov_b32 m0, s63
	ds_read_u16 v171, v171
	ds_read_u16 v215, v172
	ds_read_u16 v216, v173
	ds_read_u16 v214, v214
	v_lshl_add_u64 v[172:173], v[138:139], 0, s[0:1]
	s_mov_b64 s[0:1], 0x1e000
	v_lshl_add_u64 v[138:139], v[138:139], 0, s[0:1]
	s_mov_b32 m0, s60
	s_mov_b64 s[0:1], 0x54000
	v_lshl_add_u64 v[138:139], v[140:141], 0, s[0:1]
	v_lshl_add_u64 v[140:141], v[138:139], 0, s[18:19]
	s_mov_b32 m0, s59
	v_lshl_add_u64 v[130:131], s[16:17], 0, v[130:131]
	global_load_lds_dwordx4 v[140:141], off
	v_lshl_add_u64 v[140:141], v[138:139], 0, s[20:21]
	s_mov_b32 m0, s58
	v_lshl_add_u64 v[138:139], v[138:139], 0, s[22:23]
	global_load_lds_dwordx4 v[140:141], off
	s_mov_b32 m0, s57
	s_mov_b64 s[0:1], 0x3800
	global_load_lds_dwordx4 v[138:139], off
	v_lshl_add_u64 v[130:131], v[130:131], 0, s[0:1]
	s_add_i32 m0, s3, 0x21800
	s_waitcnt lgkmcnt(0)
	v_mov_b32_e32 v172, v216
	global_load_lds_dword v[130:131], off
	s_waitcnt vmcnt(6)
	s_waitcnt lgkmcnt(0)
	v_mov_b32_e32 v130, v171
	v_mov_b32_e32 v131, v215
	v_mov_b32_e32 v217, v214
	s_barrier
	v_mov_b32_e32 v240, 0x7f7f7f7f
	s_nop 1
	v_mfma_scale_f32_16x16x128_f8f6f4 v[126:129], v[154:157], v[142:147], v[126:129], v240, v130 op_sel_hi:[0,0,0] cbsz:4 blgp:2
	v_mfma_scale_f32_16x16x128_f8f6f4 v[122:125], v[186:189], v[142:147], v[122:125], v240, v130 op_sel_hi:[0,0,0] cbsz:4 blgp:2
	v_mfma_scale_f32_16x16x128_f8f6f4 v[114:117], v[190:193], v[142:147], v[114:117], v240, v130 op_sel_hi:[0,0,0] cbsz:4 blgp:2
	v_mfma_scale_f32_16x16x128_f8f6f4 v[102:105], v[194:197], v[142:147], v[102:105], v240, v130 op_sel_hi:[0,0,0] cbsz:4 blgp:2
	v_mfma_scale_f32_16x16x128_f8f6f4 v[86:89], v[198:201], v[142:147], v[86:89], v240, v130 op_sel_hi:[0,0,0] cbsz:4 blgp:2
	v_mfma_scale_f32_16x16x128_f8f6f4 v[70:73], v[202:205], v[142:147], v[70:73], v240, v130 op_sel_hi:[0,0,0] cbsz:4 blgp:2
	v_mfma_scale_f32_16x16x128_f8f6f4 v[54:57], v[206:209], v[142:147], v[54:57], v240, v130 op_sel_hi:[0,0,0] cbsz:4 blgp:2
	v_mfma_scale_f32_16x16x128_f8f6f4 v[38:41], v[210:213], v[142:147], v[38:41], v240, v130 op_sel_hi:[0,0,0] cbsz:4 blgp:2
	v_mfma_scale_f32_16x16x128_f8f6f4 v[118:121], v[154:157], v[148:153], v[118:121], v240, v131 op_sel_hi:[0,0,0] cbsz:4 blgp:2
	v_mfma_scale_f32_16x16x128_f8f6f4 v[110:113], v[186:189], v[148:153], v[110:113], v240, v131 op_sel_hi:[0,0,0] cbsz:4 blgp:2
	v_mfma_scale_f32_16x16x128_f8f6f4 v[98:101], v[190:193], v[148:153], v[98:101], v240, v131 op_sel_hi:[0,0,0] cbsz:4 blgp:2
	v_mfma_scale_f32_16x16x128_f8f6f4 v[82:85], v[194:197], v[148:153], v[82:85], v240, v131 op_sel_hi:[0,0,0] cbsz:4 blgp:2
	v_mfma_scale_f32_16x16x128_f8f6f4 v[66:69], v[198:201], v[148:153], v[66:69], v240, v131 op_sel_hi:[0,0,0] cbsz:4 blgp:2
	v_mfma_scale_f32_16x16x128_f8f6f4 v[50:53], v[202:205], v[148:153], v[50:53], v240, v131 op_sel_hi:[0,0,0] cbsz:4 blgp:2
	v_mfma_scale_f32_16x16x128_f8f6f4 v[138:141], v[210:213], v[148:153], v[22:25], v240, v131 op_sel_hi:[0,0,0] cbsz:4 blgp:2
	v_mfma_scale_f32_16x16x128_f8f6f4 v[106:109], v[154:157], v[174:179], v[106:109], v240, v172 op_sel_hi:[0,0,0] cbsz:4 blgp:2
	v_mfma_scale_f32_16x16x128_f8f6f4 v[94:97], v[186:189], v[174:179], v[94:97], v240, v172 op_sel_hi:[0,0,0] cbsz:4 blgp:2
	v_mfma_scale_f32_16x16x128_f8f6f4 v[78:81], v[190:193], v[174:179], v[78:81], v240, v172 op_sel_hi:[0,0,0] cbsz:4 blgp:2
	v_mfma_scale_f32_16x16x128_f8f6f4 v[62:65], v[194:197], v[174:179], v[62:65], v240, v172 op_sel_hi:[0,0,0] cbsz:4 blgp:2
	v_mfma_scale_f32_16x16x128_f8f6f4 v[46:49], v[198:201], v[174:179], v[46:49], v240, v172 op_sel_hi:[0,0,0] cbsz:4 blgp:2
	v_mfma_scale_f32_16x16x128_f8f6f4 v[30:33], v[202:205], v[174:179], v[30:33], v240, v172 op_sel_hi:[0,0,0] cbsz:4 blgp:2
	v_mfma_scale_f32_16x16x128_f8f6f4 v[142:145], v[206:209], v[174:179], v[18:21], v240, v172 op_sel_hi:[0,0,0] cbsz:4 blgp:2
	v_mfma_scale_f32_16x16x128_f8f6f4 v[90:93], v[154:157], v[180:185], v[90:93], v240, v217 op_sel_hi:[0,0,0] cbsz:4 blgp:2
	v_mfma_scale_f32_16x16x128_f8f6f4 v[74:77], v[186:189], v[180:185], v[74:77], v240, v217 op_sel_hi:[0,0,0] cbsz:4 blgp:2
	v_mfma_scale_f32_16x16x128_f8f6f4 v[58:61], v[190:193], v[180:185], v[58:61], v240, v217 op_sel_hi:[0,0,0] cbsz:4 blgp:2
	v_mfma_scale_f32_16x16x128_f8f6f4 v[26:29], v[198:201], v[180:185], v[26:29], v240, v217 op_sel_hi:[0,0,0] cbsz:4 blgp:2
	v_mfma_scale_f32_16x16x128_f8f6f4 v[34:37], v[206:209], v[148:153], v[34:37], v240, v131 op_sel_hi:[0,0,0] cbsz:4 blgp:2
	v_mfma_scale_f32_16x16x128_f8f6f4 v[146:149], v[210:213], v[174:179], v[10:13], v240, v172 op_sel_hi:[0,0,0] cbsz:4 blgp:2
	v_mfma_scale_f32_16x16x128_f8f6f4 v[42:45], v[194:197], v[180:185], v[42:45], v240, v217 op_sel_hi:[0,0,0] cbsz:4 blgp:2
	v_mfma_scale_f32_16x16x128_f8f6f4 v[150:153], v[202:205], v[180:185], v[14:17], v240, v217 op_sel_hi:[0,0,0] cbsz:4 blgp:2
	v_mfma_scale_f32_16x16x128_f8f6f4 v[172:175], v[206:209], v[180:185], v[6:9], v240, v217 op_sel_hi:[0,0,0] cbsz:4 blgp:2
	v_mfma_scale_f32_16x16x128_f8f6f4 v[176:179], v[210:213], v[180:185], v[2:5], v240, v217 op_sel_hi:[0,0,0] cbsz:4 blgp:2
	s_barrier
	ds_read_b64 v[2:3], v167
	ds_read_b64 v[4:5], v167 offset:8
	ds_read_b64 v[6:7], v167 offset:16
	ds_read_b64 v[8:9], v170
	ds_read_b64 v[10:11], v170 offset:8
	ds_read_b64 v[12:13], v170 offset:16
	ds_read_b64 v[14:15], v169
	ds_read_b64 v[16:17], v169 offset:8
	ds_read_b64 v[18:19], v169 offset:16
	s_mov_b64 s[0:1], 0x55800
	s_mov_b32 m0, s54
	ds_read_b64 v[20:21], v168
	ds_read_b64 v[22:23], v168 offset:8
	ds_read_b64 v[24:25], v168 offset:16
	v_lshl_add_u64 v[130:131], v[132:133], 0, s[0:1]
	global_load_lds_dwordx4 v[130:131], off
	v_lshl_add_u64 v[130:131], v[134:135], 0, s[0:1]
	s_mov_b32 m0, s52
	v_lshrrev_b32_e32 v167, 8, v216
	global_load_lds_dwordx4 v[130:131], off
	v_lshl_add_u64 v[130:131], v[136:137], 0, s[0:1]
	s_mov_b32 m0, s51
	v_lshrrev_b32_e32 v168, 8, v214
	global_load_lds_dwordx4 v[130:131], off
	s_waitcnt vmcnt(3)
	s_waitcnt lgkmcnt(0)
	v_lshrrev_b32_e32 v130, 8, v171
	v_lshrrev_b32_e32 v131, 8, v215
	s_barrier
	v_mfma_scale_f32_16x16x128_f8f6f4 v[126:129], v[154:157], v[2:7], v[126:129], v240, v130 op_sel_hi:[0,0,0] cbsz:4 blgp:2
	v_mfma_scale_f32_16x16x128_f8f6f4 v[122:125], v[186:189], v[2:7], v[122:125], v240, v130 op_sel_hi:[0,0,0] cbsz:4 blgp:2
	v_mfma_scale_f32_16x16x128_f8f6f4 v[114:117], v[190:193], v[2:7], v[114:117], v240, v130 op_sel_hi:[0,0,0] cbsz:4 blgp:2
	v_mfma_scale_f32_16x16x128_f8f6f4 v[102:105], v[194:197], v[2:7], v[102:105], v240, v130 op_sel_hi:[0,0,0] cbsz:4 blgp:2
	v_mfma_scale_f32_16x16x128_f8f6f4 v[86:89], v[198:201], v[2:7], v[86:89], v240, v130 op_sel_hi:[0,0,0] cbsz:4 blgp:2
	v_mfma_scale_f32_16x16x128_f8f6f4 v[70:73], v[202:205], v[2:7], v[70:73], v240, v130 op_sel_hi:[0,0,0] cbsz:4 blgp:2
	v_mfma_scale_f32_16x16x128_f8f6f4 v[54:57], v[206:209], v[2:7], v[54:57], v240, v130 op_sel_hi:[0,0,0] cbsz:4 blgp:2
	v_mfma_scale_f32_16x16x128_f8f6f4 v[38:41], v[210:213], v[2:7], v[38:41], v240, v130 op_sel_hi:[0,0,0] cbsz:4 blgp:2
	v_mfma_scale_f32_16x16x128_f8f6f4 v[118:121], v[154:157], v[8:13], v[118:121], v240, v131 op_sel_hi:[0,0,0] cbsz:4 blgp:2
	v_mfma_scale_f32_16x16x128_f8f6f4 v[110:113], v[186:189], v[8:13], v[110:113], v240, v131 op_sel_hi:[0,0,0] cbsz:4 blgp:2
	v_mfma_scale_f32_16x16x128_f8f6f4 v[98:101], v[190:193], v[8:13], v[98:101], v240, v131 op_sel_hi:[0,0,0] cbsz:4 blgp:2
	v_mfma_scale_f32_16x16x128_f8f6f4 v[82:85], v[194:197], v[8:13], v[82:85], v240, v131 op_sel_hi:[0,0,0] cbsz:4 blgp:2
	v_mfma_scale_f32_16x16x128_f8f6f4 v[66:69], v[198:201], v[8:13], v[66:69], v240, v131 op_sel_hi:[0,0,0] cbsz:4 blgp:2
	v_mfma_scale_f32_16x16x128_f8f6f4 v[50:53], v[202:205], v[8:13], v[50:53], v240, v131 op_sel_hi:[0,0,0] cbsz:4 blgp:2
	v_mfma_scale_f32_16x16x128_f8f6f4 v[34:37], v[206:209], v[8:13], v[34:37], v240, v131 op_sel_hi:[0,0,0] cbsz:4 blgp:2
	v_mfma_scale_f32_16x16x128_f8f6f4 v[130:133], v[210:213], v[8:13], v[138:141], v240, v131 op_sel_hi:[0,0,0] cbsz:4 blgp:2
	v_mfma_scale_f32_16x16x128_f8f6f4 v[106:109], v[154:157], v[14:19], v[106:109], v240, v167 op_sel_hi:[0,0,0] cbsz:4 blgp:2
	v_mfma_scale_f32_16x16x128_f8f6f4 v[94:97], v[186:189], v[14:19], v[94:97], v240, v167 op_sel_hi:[0,0,0] cbsz:4 blgp:2
	v_mfma_scale_f32_16x16x128_f8f6f4 v[78:81], v[190:193], v[14:19], v[78:81], v240, v167 op_sel_hi:[0,0,0] cbsz:4 blgp:2
	v_mfma_scale_f32_16x16x128_f8f6f4 v[62:65], v[194:197], v[14:19], v[62:65], v240, v167 op_sel_hi:[0,0,0] cbsz:4 blgp:2
	v_mfma_scale_f32_16x16x128_f8f6f4 v[46:49], v[198:201], v[14:19], v[46:49], v240, v167 op_sel_hi:[0,0,0] cbsz:4 blgp:2
	v_mfma_scale_f32_16x16x128_f8f6f4 v[30:33], v[202:205], v[14:19], v[30:33], v240, v167 op_sel_hi:[0,0,0] cbsz:4 blgp:2
	v_mfma_scale_f32_16x16x128_f8f6f4 v[134:137], v[206:209], v[14:19], v[142:145], v240, v167 op_sel_hi:[0,0,0] cbsz:4 blgp:2
	v_mfma_scale_f32_16x16x128_f8f6f4 v[138:141], v[210:213], v[14:19], v[146:149], v240, v167 op_sel_hi:[0,0,0] cbsz:4 blgp:2
	v_mfma_scale_f32_16x16x128_f8f6f4 v[90:93], v[154:157], v[20:25], v[90:93], v240, v168 op_sel_hi:[0,0,0] cbsz:4 blgp:2
	v_mfma_scale_f32_16x16x128_f8f6f4 v[74:77], v[186:189], v[20:25], v[74:77], v240, v168 op_sel_hi:[0,0,0] cbsz:4 blgp:2
	v_mfma_scale_f32_16x16x128_f8f6f4 v[58:61], v[190:193], v[20:25], v[58:61], v240, v168 op_sel_hi:[0,0,0] cbsz:4 blgp:2
	v_mfma_scale_f32_16x16x128_f8f6f4 v[26:29], v[198:201], v[20:25], v[26:29], v240, v168 op_sel_hi:[0,0,0] cbsz:4 blgp:2
	v_mfma_scale_f32_16x16x128_f8f6f4 v[142:145], v[202:205], v[20:25], v[150:153], v240, v168 op_sel_hi:[0,0,0] cbsz:4 blgp:2
	v_mfma_scale_f32_16x16x128_f8f6f4 v[42:45], v[194:197], v[20:25], v[42:45], v240, v168 op_sel_hi:[0,0,0] cbsz:4 blgp:2
	v_mfma_scale_f32_16x16x128_f8f6f4 v[146:149], v[206:209], v[20:25], v[172:175], v240, v168 op_sel_hi:[0,0,0] cbsz:4 blgp:2
	v_mfma_scale_f32_16x16x128_f8f6f4 v[150:153], v[210:213], v[20:25], v[176:179], v240, v168 op_sel_hi:[0,0,0] cbsz:4 blgp:2
	s_barrier
	ds_read_b128 v[154:157], v166
	ds_read_b128 v[168:171], v166 offset:256
	ds_read_b128 v[172:175], v166 offset:512
	ds_read_b128 v[176:179], v166 offset:768
	ds_read_b128 v[180:183], v166 offset:1024
	ds_read_b128 v[184:187], v166 offset:1280
	ds_read_b128 v[188:191], v166 offset:1536
	ds_read_b128 v[192:195], v166 offset:1792
	ds_read_b64 v[2:3], v162
	ds_read_b64 v[4:5], v162 offset:8
	ds_read_b64 v[6:7], v162 offset:16
	ds_read_b64 v[8:9], v165
	ds_read_b64 v[10:11], v165 offset:8
	ds_read_b64 v[12:13], v165 offset:16
	ds_read_b64 v[14:15], v164
	ds_read_b64 v[16:17], v164 offset:8
	ds_read_b64 v[18:19], v164 offset:16
	ds_read_b64 v[20:21], v163
	ds_read_b64 v[22:23], v163 offset:8
	ds_read_b64 v[24:25], v163 offset:16
	v_add_u32_e32 v162, 0x21800, v161
	v_add_u32_e32 v163, 0x21820, v161
	v_add_u32_e32 v164, 0x21840, v161
	v_add_u32_e32 v161, 0x21860, v161
	ds_read_u16 v166, v162
	ds_read_u16 v167, v163
	ds_read_u16 v241, v164
	ds_read_u16 v161, v161
	s_waitcnt vmcnt(0)
	s_waitcnt lgkmcnt(0)
	s_waitcnt lgkmcnt(0)
	v_mov_b32_e32 v162, v166
	v_mov_b32_e32 v200, v167
	v_mov_b32_e32 v216, v241
	v_mov_b32_e32 v242, v161
	s_barrier
	v_mfma_scale_f32_16x16x128_f8f6f4 v[126:129], v[154:157], v[2:7], v[126:129], v240, v162 op_sel_hi:[0,0,0] cbsz:4 blgp:2
	v_mfma_scale_f32_16x16x128_f8f6f4 v[122:125], v[168:171], v[2:7], v[122:125], v240, v162 op_sel_hi:[0,0,0] cbsz:4 blgp:2
	v_mfma_scale_f32_16x16x128_f8f6f4 v[114:117], v[172:175], v[2:7], v[114:117], v240, v162 op_sel_hi:[0,0,0] cbsz:4 blgp:2
	v_mfma_scale_f32_16x16x128_f8f6f4 v[102:105], v[176:179], v[2:7], v[102:105], v240, v162 op_sel_hi:[0,0,0] cbsz:4 blgp:2
	v_mfma_scale_f32_16x16x128_f8f6f4 v[86:89], v[180:183], v[2:7], v[86:89], v240, v162 op_sel_hi:[0,0,0] cbsz:4 blgp:2
	v_mfma_scale_f32_16x16x128_f8f6f4 v[70:73], v[184:187], v[2:7], v[70:73], v240, v162 op_sel_hi:[0,0,0] cbsz:4 blgp:2
	v_mfma_scale_f32_16x16x128_f8f6f4 v[54:57], v[188:191], v[2:7], v[54:57], v240, v162 op_sel_hi:[0,0,0] cbsz:4 blgp:2
	v_mfma_scale_f32_16x16x128_f8f6f4 v[2:5], v[192:195], v[2:7], v[38:41], v240, v162 op_sel_hi:[0,0,0] cbsz:4 blgp:2
	v_mfma_scale_f32_16x16x128_f8f6f4 v[118:121], v[154:157], v[8:13], v[118:121], v240, v200 op_sel_hi:[0,0,0] cbsz:4 blgp:2
	v_mfma_scale_f32_16x16x128_f8f6f4 v[110:113], v[168:171], v[8:13], v[110:113], v240, v200 op_sel_hi:[0,0,0] cbsz:4 blgp:2
	v_mfma_scale_f32_16x16x128_f8f6f4 v[98:101], v[172:175], v[8:13], v[98:101], v240, v200 op_sel_hi:[0,0,0] cbsz:4 blgp:2
	v_mfma_scale_f32_16x16x128_f8f6f4 v[82:85], v[176:179], v[8:13], v[82:85], v240, v200 op_sel_hi:[0,0,0] cbsz:4 blgp:2
	v_mfma_scale_f32_16x16x128_f8f6f4 v[66:69], v[180:183], v[8:13], v[66:69], v240, v200 op_sel_hi:[0,0,0] cbsz:4 blgp:2
	v_mfma_scale_f32_16x16x128_f8f6f4 v[106:109], v[154:157], v[14:19], v[106:109], v240, v216 op_sel_hi:[0,0,0] cbsz:4 blgp:2
	v_mfma_scale_f32_16x16x128_f8f6f4 v[94:97], v[168:171], v[14:19], v[94:97], v240, v216 op_sel_hi:[0,0,0] cbsz:4 blgp:2
	v_mfma_scale_f32_16x16x128_f8f6f4 v[78:81], v[172:175], v[14:19], v[78:81], v240, v216 op_sel_hi:[0,0,0] cbsz:4 blgp:2
	v_mfma_scale_f32_16x16x128_f8f6f4 v[62:65], v[176:179], v[14:19], v[62:65], v240, v216 op_sel_hi:[0,0,0] cbsz:4 blgp:2
	v_mfma_scale_f32_16x16x128_f8f6f4 v[74:77], v[168:171], v[20:25], v[74:77], v240, v242 op_sel_hi:[0,0,0] cbsz:4 blgp:2
	v_mfma_scale_f32_16x16x128_f8f6f4 v[58:61], v[172:175], v[20:25], v[58:61], v240, v242 op_sel_hi:[0,0,0] cbsz:4 blgp:2
	v_mfma_scale_f32_16x16x128_f8f6f4 v[162:165], v[184:187], v[8:13], v[50:53], v240, v200 op_sel_hi:[0,0,0] cbsz:4 blgp:2
	v_mfma_scale_f32_16x16x128_f8f6f4 v[196:199], v[188:191], v[8:13], v[34:37], v240, v200 op_sel_hi:[0,0,0] cbsz:4 blgp:2
	v_mfma_scale_f32_16x16x128_f8f6f4 v[200:203], v[192:195], v[8:13], v[130:133], v240, v200 op_sel_hi:[0,0,0] cbsz:4 blgp:2
	v_mfma_scale_f32_16x16x128_f8f6f4 v[204:207], v[180:183], v[14:19], v[46:49], v240, v216 op_sel_hi:[0,0,0] cbsz:4 blgp:2
	v_mfma_scale_f32_16x16x128_f8f6f4 v[208:211], v[184:187], v[14:19], v[30:33], v240, v216 op_sel_hi:[0,0,0] cbsz:4 blgp:2
	v_mfma_scale_f32_16x16x128_f8f6f4 v[212:215], v[188:191], v[14:19], v[134:137], v240, v216 op_sel_hi:[0,0,0] cbsz:4 blgp:2
	v_mfma_scale_f32_16x16x128_f8f6f4 v[216:219], v[192:195], v[14:19], v[138:141], v240, v216 op_sel_hi:[0,0,0] cbsz:4 blgp:2
	v_mfma_scale_f32_16x16x128_f8f6f4 v[220:223], v[154:157], v[20:25], v[90:93], v240, v242 op_sel_hi:[0,0,0] cbsz:4 blgp:2
	v_mfma_scale_f32_16x16x128_f8f6f4 v[224:227], v[176:179], v[20:25], v[42:45], v240, v242 op_sel_hi:[0,0,0] cbsz:4 blgp:2
	v_mfma_scale_f32_16x16x128_f8f6f4 v[228:231], v[180:183], v[20:25], v[26:29], v240, v242 op_sel_hi:[0,0,0] cbsz:4 blgp:2
	v_mfma_scale_f32_16x16x128_f8f6f4 v[232:235], v[184:187], v[20:25], v[142:145], v240, v242 op_sel_hi:[0,0,0] cbsz:4 blgp:2
	v_mfma_scale_f32_16x16x128_f8f6f4 v[236:239], v[188:191], v[20:25], v[146:149], v240, v242 op_sel_hi:[0,0,0] cbsz:4 blgp:2
	v_mfma_scale_f32_16x16x128_f8f6f4 v[150:153], v[192:195], v[20:25], v[150:153], v240, v242 op_sel_hi:[0,0,0] cbsz:4 blgp:2
	s_barrier
	ds_read_b64 v[34:35], v1
	ds_read_b64 v[36:37], v1 offset:8
	ds_read_b64 v[38:39], v1 offset:16
	ds_read_b64 v[40:41], v160
	ds_read_b64 v[42:43], v160 offset:8
	ds_read_b64 v[44:45], v160 offset:16
	ds_read_b64 v[46:47], v159
	ds_read_b64 v[48:49], v159 offset:8
	ds_read_b64 v[50:51], v159 offset:16
	ds_read_b64 v[144:145], v158
	ds_read_b64 v[146:147], v158 offset:8
	ds_read_b64 v[148:149], v158 offset:16
	s_waitcnt lgkmcnt(0)
	v_lshrrev_b32_e32 v1, 8, v166
	v_lshrrev_b32_e32 v52, 8, v167
	v_lshrrev_b32_e32 v53, 8, v241
	v_lshrrev_b32_e32 v158, 8, v161
	s_barrier
	v_mfma_scale_f32_16x16x128_f8f6f4 v[30:33], v[154:157], v[34:39], v[126:129], v240, v1 op_sel_hi:[0,0,0] cbsz:4 blgp:2
	v_mfma_scale_f32_16x16x128_f8f6f4 v[22:25], v[168:171], v[34:39], v[122:125], v240, v1 op_sel_hi:[0,0,0] cbsz:4 blgp:2
	v_mfma_scale_f32_16x16x128_f8f6f4 v[14:17], v[172:175], v[34:39], v[114:117], v240, v1 op_sel_hi:[0,0,0] cbsz:4 blgp:2
	v_mfma_scale_f32_16x16x128_f8f6f4 v[6:9], v[176:179], v[34:39], v[102:105], v240, v1 op_sel_hi:[0,0,0] cbsz:4 blgp:2
	v_mfma_scale_f32_16x16x128_f8f6f4 v[26:29], v[180:183], v[34:39], v[86:89], v240, v1 op_sel_hi:[0,0,0] cbsz:4 blgp:2
	v_mfma_scale_f32_16x16x128_f8f6f4 v[18:21], v[184:187], v[34:39], v[70:73], v240, v1 op_sel_hi:[0,0,0] cbsz:4 blgp:2
	v_mfma_scale_f32_16x16x128_f8f6f4 v[10:13], v[188:191], v[34:39], v[54:57], v240, v1 op_sel_hi:[0,0,0] cbsz:4 blgp:2
	v_mfma_scale_f32_16x16x128_f8f6f4 v[2:5], v[192:195], v[34:39], v[2:5], v240, v1 op_sel_hi:[0,0,0] cbsz:4 blgp:2
	v_mfma_scale_f32_16x16x128_f8f6f4 v[132:135], v[154:157], v[40:45], v[118:121], v240, v52 op_sel_hi:[0,0,0] cbsz:4 blgp:2
	v_mfma_scale_f32_16x16x128_f8f6f4 v[128:131], v[168:171], v[40:45], v[110:113], v240, v52 op_sel_hi:[0,0,0] cbsz:4 blgp:2
	v_mfma_scale_f32_16x16x128_f8f6f4 v[124:127], v[172:175], v[40:45], v[98:101], v240, v52 op_sel_hi:[0,0,0] cbsz:4 blgp:2
	v_mfma_scale_f32_16x16x128_f8f6f4 v[116:119], v[176:179], v[40:45], v[82:85], v240, v52 op_sel_hi:[0,0,0] cbsz:4 blgp:2
	v_mfma_scale_f32_16x16x128_f8f6f4 v[140:143], v[180:183], v[40:45], v[66:69], v240, v52 op_sel_hi:[0,0,0] cbsz:4 blgp:2
	v_mfma_scale_f32_16x16x128_f8f6f4 v[136:139], v[184:187], v[40:45], v[162:165], v240, v52 op_sel_hi:[0,0,0] cbsz:4 blgp:2
	v_mfma_scale_f32_16x16x128_f8f6f4 v[120:123], v[188:191], v[40:45], v[196:199], v240, v52 op_sel_hi:[0,0,0] cbsz:4 blgp:2
	v_mfma_scale_f32_16x16x128_f8f6f4 v[112:115], v[192:195], v[40:45], v[200:203], v240, v52 op_sel_hi:[0,0,0] cbsz:4 blgp:2
	v_mfma_scale_f32_16x16x128_f8f6f4 v[100:103], v[154:157], v[46:51], v[106:109], v240, v53 op_sel_hi:[0,0,0] cbsz:4 blgp:2
	v_mfma_scale_f32_16x16x128_f8f6f4 v[96:99], v[168:171], v[46:51], v[94:97], v240, v53 op_sel_hi:[0,0,0] cbsz:4 blgp:2
	v_mfma_scale_f32_16x16x128_f8f6f4 v[92:95], v[172:175], v[46:51], v[78:81], v240, v53 op_sel_hi:[0,0,0] cbsz:4 blgp:2
	v_mfma_scale_f32_16x16x128_f8f6f4 v[84:87], v[176:179], v[46:51], v[62:65], v240, v53 op_sel_hi:[0,0,0] cbsz:4 blgp:2
	v_mfma_scale_f32_16x16x128_f8f6f4 v[108:111], v[180:183], v[46:51], v[204:207], v240, v53 op_sel_hi:[0,0,0] cbsz:4 blgp:2
	v_mfma_scale_f32_16x16x128_f8f6f4 v[104:107], v[184:187], v[46:51], v[208:211], v240, v53 op_sel_hi:[0,0,0] cbsz:4 blgp:2
	v_mfma_scale_f32_16x16x128_f8f6f4 v[88:91], v[188:191], v[46:51], v[212:215], v240, v53 op_sel_hi:[0,0,0] cbsz:4 blgp:2
	v_mfma_scale_f32_16x16x128_f8f6f4 v[80:83], v[192:195], v[46:51], v[216:219], v240, v53 op_sel_hi:[0,0,0] cbsz:4 blgp:2
	v_mfma_scale_f32_16x16x128_f8f6f4 v[68:71], v[154:157], v[144:149], v[220:223], v240, v158 op_sel_hi:[0,0,0] cbsz:4 blgp:2
	v_mfma_scale_f32_16x16x128_f8f6f4 v[64:67], v[168:171], v[144:149], v[74:77], v240, v158 op_sel_hi:[0,0,0] cbsz:4 blgp:2
	v_mfma_scale_f32_16x16x128_f8f6f4 v[60:63], v[172:175], v[144:149], v[58:61], v240, v158 op_sel_hi:[0,0,0] cbsz:4 blgp:2
	v_mfma_scale_f32_16x16x128_f8f6f4 v[52:55], v[176:179], v[144:149], v[224:227], v240, v158 op_sel_hi:[0,0,0] cbsz:4 blgp:2
	v_mfma_scale_f32_16x16x128_f8f6f4 v[76:79], v[180:183], v[144:149], v[228:231], v240, v158 op_sel_hi:[0,0,0] cbsz:4 blgp:2
	v_mfma_scale_f32_16x16x128_f8f6f4 v[72:75], v[184:187], v[144:149], v[232:235], v240, v158 op_sel_hi:[0,0,0] cbsz:4 blgp:2
	v_mfma_scale_f32_16x16x128_f8f6f4 v[56:59], v[188:191], v[144:149], v[236:239], v240, v158 op_sel_hi:[0,0,0] cbsz:4 blgp:2
	v_mfma_scale_f32_16x16x128_f8f6f4 v[48:51], v[192:195], v[144:149], v[150:153], v240, v158 op_sel_hi:[0,0,0] cbsz:4 blgp:2
	s_barrier
	s_cmpk_gt_u32 s33, 0xff
	s_cbranch_scc1 .LBB2_6
	s_barrier

.LBB3_2:
	s_lshl_b32 s0, s39, 15
	s_add_i32 s0, s40, s0
	s_add_i32 s39, s0, 0x2000
	s_lshl_b32 s0, s41, 15
	v_bfe_u32 v3, v0, 4, 1
	s_add_i32 s0, s49, s0
	s_add_i32 s40, s0, 0x2000
	v_and_b32_e32 v8, 15, v0
	v_lshlrev_b32_e32 v10, 8, v3
	v_lshlrev_b32_e32 v3, 9, v3
	s_and_b32 s0, s33, 0xc0
	v_lshrrev_b32_e32 v1, 5, v1
	v_or3_b32 v3, s0, v3, v8
	v_lshlrev_b32_e32 v9, 15, v1
	v_lshl_add_u32 v11, s27, 7, v10
	v_mul_u32_u24_e32 v3, 24, v3
	s_waitcnt vmcnt(5)
	v_or_b32_e32 v11, v11, v8
	v_or3_b32 v8, v10, s0, v8
	v_or_b32_e32 v3, v3, v9
	s_add_i32 s41, 0, 0x10000
	s_addk_i32 s50, 0x2000
	v_lshl_add_u32 v11, v11, 4, v9
	v_lshlrev_b32_e32 v1, 10, v1
	v_lshlrev_b32_e32 v8, 1, v8
	v_add_u32_e32 v9, s41, v3
	s_barrier
	s_barrier
	s_add_u32 s72, s4, s22
	s_addc_u32 s73, s5, s23
	s_add_u32 s72, s72, s26
	s_addc_u32 s73, s73, 0
	s_add_u32 s72, s72, 0x8000
	s_addc_u32 s73, s73, 0
	s_add_u32 s74, s72, 0x4000
	s_addc_u32 s75, s73, 0
	s_add_u32 s76, s6, s24
	s_addc_u32 s77, s7, s25
	s_add_u32 s76, s76, 0xc000
	s_addc_u32 s77, s77, 0
	s_add_u32 s78, s76, 0xc000
	s_addc_u32 s79, s77, 0
	s_add_u32 s80, s14, s9
	s_addc_u32 s81, s15, 0
	s_add_u32 s80, s80, 0x800
	s_addc_u32 s81, s81, 0
	s_add_i32 s0, s38, s37
	s_add_i32 s0, s0, s26
	s_mulk_i32 s36, 0x1800
	s_sub_i32 s0, s0, s36
	s_addk_i32 s0, 0x4000
	v_lshl_add_u64 v[6:7], s[24:25], 0, v[6:7]
	s_ashr_i32 s1, s0, 31
	v_lshl_add_u64 v[142:143], v[6:7], 0, s[0:1]
	s_add_i32 s0, s35, s34
	s_add_i32 s0, s0, s26
	s_mulk_i32 s31, 0x1800
	s_sub_i32 s0, s0, s31
	s_addk_i32 s0, 0x2000
	s_ashr_i32 s1, s0, 31
	v_lshl_add_u64 v[144:145], v[6:7], 0, s[0:1]
	s_add_i32 s0, s30, s29
	s_add_i32 s0, s0, s26
	s_mulk_i32 s28, 0x1800
	s_sub_i32 s0, s0, s28
	s_ashr_i32 s1, s0, 31
	v_lshl_add_u64 v[146:147], v[6:7], 0, s[0:1]
	s_add_u32 s0, s4, s22
	s_addc_u32 s1, s5, s23
	v_lshl_add_u64 v[4:5], s[0:1], 0, v[4:5]
	s_mov_b64 s[0:1], 0xa000
	v_add_u32_e32 v3, 0, v3
	v_add3_u32 v248, 0, v8, v1
	v_lshl_add_u64 v[148:149], v[4:5], 0, s[0:1]
	s_movk_i32 s0, 0xa000
	s_movk_i32 s4, 0xc000
	s_add_i32 s57, s41, s50
	s_add_i32 s56, s41, s39
	s_add_i32 s55, s41, s40
	s_movk_i32 s28, 0xe000
	v_add_u32_e32 v171, 0x2000, v3
	v_add_u32_e32 v167, 0x3800, v3
	v_add_u32_e32 v162, 0x2000, v9
	v_add_u32_e32 v1, 0x3800, v9
	v_add_u32_e32 v174, 0x2180, v3
	v_add_u32_e32 v173, 0x2300, v3
	v_add_u32_e32 v172, 0x2480, v3
	v_add_u32_e32 v170, 0x3980, v3
	v_add_u32_e32 v169, 0x3b00, v3
	v_add_u32_e32 v168, 0x3c80, v3
	v_add_u32_e32 v165, 0x2180, v9
	v_add_u32_e32 v164, 0x2300, v9
	v_add_u32_e32 v163, 0x2480, v9
	v_add_u32_e32 v160, 0x3980, v9
	v_add_u32_e32 v159, 0x3b00, v9
	v_add_u32_e32 v158, 0x3c80, v9
	s_mov_b32 s59, -2
	s_movk_i32 s60, 0x1000
	v_add_u32_e32 v175, 0, v11
	s_mov_b32 s1, -1
	s_add_i32 s61, s41, s26
	s_mov_b32 s5, -1
	s_add_i32 s58, s13, 0x18000
	s_mov_b64 s[22:23], 0xc000
	s_mov_b64 s[24:25], 0x3000800
	s_mov_b64 s[26:27], 0xd800
	s_add_i32 s52, s57, 0x1800
	s_add_i32 s50, s56, 0x1800
	s_add_i32 s49, s55, 0x1800
	v_add_u32_e32 v166, s41, v11
	s_mov_b32 s29, -1
	s_mov_b64 s[30:31], 0x18000
	s_mov_b64 s[34:35], 0x3001000
	s_mov_b64 s[36:37], 0x19800
	s_mov_b64 s[38:39], 0x1000
	s_mov_b64 s[40:41], 0x8000
	v_mov_b32_e32 v3, v2
	v_mov_b32_e32 v4, v2
	v_mov_b32_e32 v5, v2
	v_mov_b32_e32 v10, v2
	v_mov_b32_e32 v11, v2
	v_mov_b32_e32 v12, v2
	v_mov_b32_e32 v13, v2
	v_mov_b32_e32 v22, v2
	v_mov_b32_e32 v23, v2
	v_mov_b32_e32 v24, v2
	v_mov_b32_e32 v25, v2
	v_mov_b32_e32 v38, v2
	v_mov_b32_e32 v39, v2
	v_mov_b32_e32 v40, v2
	v_mov_b32_e32 v41, v2
	v_mov_b32_e32 v6, v2
	v_mov_b32_e32 v7, v2
	v_mov_b32_e32 v8, v2
	v_mov_b32_e32 v9, v2
	v_mov_b32_e32 v18, v2
	v_mov_b32_e32 v19, v2
	v_mov_b32_e32 v20, v2
	v_mov_b32_e32 v21, v2
	v_mov_b32_e32 v34, v2
	v_mov_b32_e32 v35, v2
	v_mov_b32_e32 v36, v2
	v_mov_b32_e32 v37, v2
	v_mov_b32_e32 v54, v2
	v_mov_b32_e32 v55, v2
	v_mov_b32_e32 v56, v2
	v_mov_b32_e32 v57, v2
	v_mov_b32_e32 v14, v2
	v_mov_b32_e32 v15, v2
	v_mov_b32_e32 v16, v2
	v_mov_b32_e32 v17, v2
	v_mov_b32_e32 v30, v2
	v_mov_b32_e32 v31, v2
	v_mov_b32_e32 v32, v2
	v_mov_b32_e32 v33, v2
	v_mov_b32_e32 v50, v2
	v_mov_b32_e32 v51, v2
	v_mov_b32_e32 v52, v2
	v_mov_b32_e32 v53, v2
	v_mov_b32_e32 v70, v2
	v_mov_b32_e32 v71, v2
	v_mov_b32_e32 v72, v2
	v_mov_b32_e32 v73, v2
	v_mov_b32_e32 v26, v2
	v_mov_b32_e32 v27, v2
	v_mov_b32_e32 v28, v2
	v_mov_b32_e32 v29, v2
	v_mov_b32_e32 v46, v2
	v_mov_b32_e32 v47, v2
	v_mov_b32_e32 v48, v2
	v_mov_b32_e32 v49, v2
	v_mov_b32_e32 v66, v2
	v_mov_b32_e32 v67, v2
	v_mov_b32_e32 v68, v2
	v_mov_b32_e32 v69, v2
	v_mov_b32_e32 v86, v2
	v_mov_b32_e32 v87, v2
	v_mov_b32_e32 v88, v2
	v_mov_b32_e32 v89, v2
	v_mov_b32_e32 v42, v2
	v_mov_b32_e32 v43, v2
	v_mov_b32_e32 v44, v2
	v_mov_b32_e32 v45, v2
	v_mov_b32_e32 v62, v2
	v_mov_b32_e32 v63, v2
	v_mov_b32_e32 v64, v2
	v_mov_b32_e32 v65, v2
	v_mov_b32_e32 v82, v2
	v_mov_b32_e32 v83, v2
	v_mov_b32_e32 v84, v2
	v_mov_b32_e32 v85, v2
	v_mov_b32_e32 v102, v2
	v_mov_b32_e32 v103, v2
	v_mov_b32_e32 v104, v2
	v_mov_b32_e32 v105, v2
	v_mov_b32_e32 v58, v2
	v_mov_b32_e32 v59, v2
	v_mov_b32_e32 v60, v2
	v_mov_b32_e32 v61, v2
	v_mov_b32_e32 v78, v2
	v_mov_b32_e32 v79, v2
	v_mov_b32_e32 v80, v2
	v_mov_b32_e32 v81, v2
	v_mov_b32_e32 v98, v2
	v_mov_b32_e32 v99, v2
	v_mov_b32_e32 v100, v2
	v_mov_b32_e32 v101, v2
	v_mov_b32_e32 v114, v2
	v_mov_b32_e32 v115, v2
	v_mov_b32_e32 v116, v2
	v_mov_b32_e32 v117, v2
	v_mov_b32_e32 v74, v2
	v_mov_b32_e32 v75, v2
	v_mov_b32_e32 v76, v2
	v_mov_b32_e32 v77, v2
	v_mov_b32_e32 v94, v2
	v_mov_b32_e32 v95, v2
	v_mov_b32_e32 v96, v2
	v_mov_b32_e32 v97, v2
	v_mov_b32_e32 v110, v2
	v_mov_b32_e32 v111, v2
	v_mov_b32_e32 v112, v2
	v_mov_b32_e32 v113, v2
	v_mov_b32_e32 v122, v2
	v_mov_b32_e32 v123, v2
	v_mov_b32_e32 v124, v2
	v_mov_b32_e32 v125, v2
	v_mov_b32_e32 v90, v2
	v_mov_b32_e32 v91, v2
	v_mov_b32_e32 v92, v2
	v_mov_b32_e32 v93, v2
	v_mov_b32_e32 v106, v2
	v_mov_b32_e32 v107, v2
	v_mov_b32_e32 v108, v2
	v_mov_b32_e32 v109, v2
	v_mov_b32_e32 v118, v2
	v_mov_b32_e32 v119, v2
	v_mov_b32_e32 v120, v2
	v_mov_b32_e32 v121, v2
	v_mov_b32_e32 v126, v2
	v_mov_b32_e32 v127, v2
	v_mov_b32_e32 v128, v2
	v_mov_b32_e32 v129, v2
	v_add_u32_e32 v176, 0x20000, v248
	v_mov_b32_e32 v177, 0x7f7f7f7f
	v_lshl_add_u64 v[150:151], s[42:43], 0, v[130:131]
	s_mov_b64 s[62:63], 0x2000
	s_mov_b64 s[64:65], 0x4000
	v_and_b32_e32 v142, 63, v0
	v_lshlrev_b32_e32 v150, 2, v142
	v_lshlrev_b32_e32 v142, 4, v142
	v_add_u32_e32 v143, 0x2000, v142
	v_add_u32_e32 v144, s16, v142
	v_add_u32_e32 v145, s18, v142
	v_add_u32_e32 v146, s20, v142
	v_add_u32_e32 v147, 0x1800, v144
	v_add_u32_e32 v148, 0x1800, v145
	v_add_u32_e32 v149, 0x1800, v146
	v_add_u32_e32 v151, 0x800, v150
	s_add_i32 s42, s60, 0xfffff000
	s_and_b32 s42, s42, 0x1000
.LBB3_3:
	ds_read_b128 v[202:205], v175
	ds_read_b128 v[206:209], v175 offset:256
	ds_read_b128 v[210:213], v175 offset:512
	ds_read_b128 v[214:217], v175 offset:768
	ds_read_b128 v[218:221], v175 offset:1024
	ds_read_b128 v[222:225], v175 offset:1280
	ds_read_b128 v[226:229], v175 offset:1536
	ds_read_b128 v[230:233], v175 offset:1792
	ds_read2_b64 v[178:181], v171 offset1:1
	ds_read2_b64 v[182:185], v171 offset0:2 offset1:48
	ds_read2_b64 v[186:189], v171 offset0:49 offset1:50
	s_mov_b32 m0, s57
	ds_read2_b64 v[190:193], v171 offset0:96 offset1:97
	global_load_lds_dwordx4 v144, s[76:77]
	s_mov_b32 m0, s56
	ds_read2_b64 v[194:197], v171 offset0:98 offset1:144
	global_load_lds_dwordx4 v145, s[76:77]
	s_mov_b32 m0, s55
	ds_read2_b64 v[198:201], v171 offset0:145 offset1:146
	global_load_lds_dwordx4 v146, s[76:77]
	v_add_u32_e32 v152, s42, v176
	ds_read_u16 v240, v152
	ds_read_u16 v241, v152 offset:32
	ds_read_u16 v242, v152 offset:64
	s_add_i32 s42, s60, 0xfffff800
	s_and_b32 s42, s42, 0x1800
	s_add_i32 m0, s48, s42
	ds_read_u16 v243, v152 offset:96
	global_load_lds_dword v150, s[80:81]
	s_waitcnt vmcnt(6)
	s_waitcnt lgkmcnt(0)
	s_barrier
	v_mfma_scale_f32_16x16x128_f8f6f4 v[126:129], v[202:205], v[178:183], v[126:129], v177, v240 op_sel_hi:[0,0,0] cbsz:4 blgp:2
	v_mfma_scale_f32_16x16x128_f8f6f4 v[122:125], v[206:209], v[178:183], v[122:125], v177, v240 op_sel_hi:[0,0,0] cbsz:4 blgp:2
	v_mfma_scale_f32_16x16x128_f8f6f4 v[114:117], v[210:213], v[178:183], v[114:117], v177, v240 op_sel_hi:[0,0,0] cbsz:4 blgp:2
	v_mfma_scale_f32_16x16x128_f8f6f4 v[102:105], v[214:217], v[178:183], v[102:105], v177, v240 op_sel_hi:[0,0,0] cbsz:4 blgp:2
	v_mfma_scale_f32_16x16x128_f8f6f4 v[86:89], v[218:221], v[178:183], v[86:89], v177, v240 op_sel_hi:[0,0,0] cbsz:4 blgp:2
	v_mfma_scale_f32_16x16x128_f8f6f4 v[70:73], v[222:225], v[178:183], v[70:73], v177, v240 op_sel_hi:[0,0,0] cbsz:4 blgp:2
	v_mfma_scale_f32_16x16x128_f8f6f4 v[54:57], v[226:229], v[178:183], v[54:57], v177, v240 op_sel_hi:[0,0,0] cbsz:4 blgp:2
	v_mfma_scale_f32_16x16x128_f8f6f4 v[38:41], v[230:233], v[178:183], v[38:41], v177, v240 op_sel_hi:[0,0,0] cbsz:4 blgp:2
	v_mfma_scale_f32_16x16x128_f8f6f4 v[118:121], v[202:205], v[184:189], v[118:121], v177, v241 op_sel_hi:[0,0,0] cbsz:4 blgp:2
	v_mfma_scale_f32_16x16x128_f8f6f4 v[110:113], v[206:209], v[184:189], v[110:113], v177, v241 op_sel_hi:[0,0,0] cbsz:4 blgp:2
	v_mfma_scale_f32_16x16x128_f8f6f4 v[98:101], v[210:213], v[184:189], v[98:101], v177, v241 op_sel_hi:[0,0,0] cbsz:4 blgp:2
	v_mfma_scale_f32_16x16x128_f8f6f4 v[82:85], v[214:217], v[184:189], v[82:85], v177, v241 op_sel_hi:[0,0,0] cbsz:4 blgp:2
	v_mfma_scale_f32_16x16x128_f8f6f4 v[66:69], v[218:221], v[184:189], v[66:69], v177, v241 op_sel_hi:[0,0,0] cbsz:4 blgp:2
	v_mfma_scale_f32_16x16x128_f8f6f4 v[50:53], v[222:225], v[184:189], v[50:53], v177, v241 op_sel_hi:[0,0,0] cbsz:4 blgp:2
	v_mfma_scale_f32_16x16x128_f8f6f4 v[34:37], v[226:229], v[184:189], v[34:37], v177, v241 op_sel_hi:[0,0,0] cbsz:4 blgp:2
	v_mfma_scale_f32_16x16x128_f8f6f4 v[106:109], v[202:205], v[190:195], v[106:109], v177, v242 op_sel_hi:[0,0,0] cbsz:4 blgp:2
	v_mfma_scale_f32_16x16x128_f8f6f4 v[94:97], v[206:209], v[190:195], v[94:97], v177, v242 op_sel_hi:[0,0,0] cbsz:4 blgp:2
	v_mfma_scale_f32_16x16x128_f8f6f4 v[78:81], v[210:213], v[190:195], v[78:81], v177, v242 op_sel_hi:[0,0,0] cbsz:4 blgp:2
	v_mfma_scale_f32_16x16x128_f8f6f4 v[62:65], v[214:217], v[190:195], v[62:65], v177, v242 op_sel_hi:[0,0,0] cbsz:4 blgp:2
	v_mfma_scale_f32_16x16x128_f8f6f4 v[46:49], v[218:221], v[190:195], v[46:49], v177, v242 op_sel_hi:[0,0,0] cbsz:4 blgp:2
	v_mfma_scale_f32_16x16x128_f8f6f4 v[30:33], v[222:225], v[190:195], v[30:33], v177, v242 op_sel_hi:[0,0,0] cbsz:4 blgp:2
	v_mfma_scale_f32_16x16x128_f8f6f4 v[90:93], v[202:205], v[196:201], v[90:93], v177, v243 op_sel_hi:[0,0,0] cbsz:4 blgp:2
	v_mfma_scale_f32_16x16x128_f8f6f4 v[74:77], v[206:209], v[196:201], v[74:77], v177, v243 op_sel_hi:[0,0,0] cbsz:4 blgp:2
	v_mfma_scale_f32_16x16x128_f8f6f4 v[58:61], v[210:213], v[196:201], v[58:61], v177, v243 op_sel_hi:[0,0,0] cbsz:4 blgp:2
	v_mfma_scale_f32_16x16x128_f8f6f4 v[42:45], v[214:217], v[196:201], v[42:45], v177, v243 op_sel_hi:[0,0,0] cbsz:4 blgp:2
	v_mfma_scale_f32_16x16x128_f8f6f4 v[26:29], v[218:221], v[196:201], v[26:29], v177, v243 op_sel_hi:[0,0,0] cbsz:4 blgp:2
	v_mfma_scale_f32_16x16x128_f8f6f4 v[178:181], v[230:233], v[184:189], v[22:25], v177, v241 op_sel_hi:[0,0,0] cbsz:4 blgp:2
	v_mfma_scale_f32_16x16x128_f8f6f4 v[182:185], v[226:229], v[190:195], v[18:21], v177, v242 op_sel_hi:[0,0,0] cbsz:4 blgp:2
	v_mfma_scale_f32_16x16x128_f8f6f4 v[186:189], v[230:233], v[190:195], v[10:13], v177, v242 op_sel_hi:[0,0,0] cbsz:4 blgp:2
	v_mfma_scale_f32_16x16x128_f8f6f4 v[190:193], v[222:225], v[196:201], v[14:17], v177, v243 op_sel_hi:[0,0,0] cbsz:4 blgp:2
	v_mfma_scale_f32_16x16x128_f8f6f4 v[234:237], v[226:229], v[196:201], v[6:9], v177, v243 op_sel_hi:[0,0,0] cbsz:4 blgp:2
	v_mfma_scale_f32_16x16x128_f8f6f4 v[194:197], v[230:233], v[196:201], v[2:5], v177, v243 op_sel_hi:[0,0,0] cbsz:4 blgp:2
	s_barrier
	ds_read2_b64 v[2:5], v167 offset1:1
	s_mov_b32 m0, s52
	ds_read2_b64 v[6:9], v167 offset0:2 offset1:48
	global_load_lds_dwordx4 v147, s[76:77]
	s_mov_b32 m0, s50
	ds_read2_b64 v[10:13], v167 offset0:49 offset1:50
	global_load_lds_dwordx4 v148, s[76:77]
	s_mov_b32 m0, s49
	ds_read2_b64 v[14:17], v167 offset0:96 offset1:97
	global_load_lds_dwordx4 v149, s[76:77]
	s_mov_b32 m0, s13
	ds_read2_b64 v[18:21], v167 offset0:98 offset1:144
	global_load_lds_dwordx4 v142, s[72:73]
	s_mov_b32 m0, s44
	ds_read2_b64 v[22:25], v167 offset0:145 offset1:146
	global_load_lds_dwordx4 v143, s[72:73]
	s_waitcnt vmcnt(5)
	s_waitcnt lgkmcnt(0)
	s_barrier
	v_mfma_scale_f32_16x16x128_f8f6f4 v[126:129], v[202:205], v[2:7], v[126:129], v177, v240 op_sel:[0,1,0] op_sel_hi:[0,0,0] cbsz:4 blgp:2
	v_mfma_scale_f32_16x16x128_f8f6f4 v[122:125], v[206:209], v[2:7], v[122:125], v177, v240 op_sel:[0,1,0] op_sel_hi:[0,0,0] cbsz:4 blgp:2
	v_mfma_scale_f32_16x16x128_f8f6f4 v[114:117], v[210:213], v[2:7], v[114:117], v177, v240 op_sel:[0,1,0] op_sel_hi:[0,0,0] cbsz:4 blgp:2
	v_mfma_scale_f32_16x16x128_f8f6f4 v[102:105], v[214:217], v[2:7], v[102:105], v177, v240 op_sel:[0,1,0] op_sel_hi:[0,0,0] cbsz:4 blgp:2
	v_mfma_scale_f32_16x16x128_f8f6f4 v[86:89], v[218:221], v[2:7], v[86:89], v177, v240 op_sel:[0,1,0] op_sel_hi:[0,0,0] cbsz:4 blgp:2
	v_mfma_scale_f32_16x16x128_f8f6f4 v[70:73], v[222:225], v[2:7], v[70:73], v177, v240 op_sel:[0,1,0] op_sel_hi:[0,0,0] cbsz:4 blgp:2
	v_mfma_scale_f32_16x16x128_f8f6f4 v[54:57], v[226:229], v[2:7], v[54:57], v177, v240 op_sel:[0,1,0] op_sel_hi:[0,0,0] cbsz:4 blgp:2
	v_mfma_scale_f32_16x16x128_f8f6f4 v[38:41], v[230:233], v[2:7], v[38:41], v177, v240 op_sel:[0,1,0] op_sel_hi:[0,0,0] cbsz:4 blgp:2
	v_mfma_scale_f32_16x16x128_f8f6f4 v[118:121], v[202:205], v[8:13], v[118:121], v177, v241 op_sel:[0,1,0] op_sel_hi:[0,0,0] cbsz:4 blgp:2
	v_mfma_scale_f32_16x16x128_f8f6f4 v[110:113], v[206:209], v[8:13], v[110:113], v177, v241 op_sel:[0,1,0] op_sel_hi:[0,0,0] cbsz:4 blgp:2
	v_mfma_scale_f32_16x16x128_f8f6f4 v[98:101], v[210:213], v[8:13], v[98:101], v177, v241 op_sel:[0,1,0] op_sel_hi:[0,0,0] cbsz:4 blgp:2
	v_mfma_scale_f32_16x16x128_f8f6f4 v[82:85], v[214:217], v[8:13], v[82:85], v177, v241 op_sel:[0,1,0] op_sel_hi:[0,0,0] cbsz:4 blgp:2
	v_mfma_scale_f32_16x16x128_f8f6f4 v[66:69], v[218:221], v[8:13], v[66:69], v177, v241 op_sel:[0,1,0] op_sel_hi:[0,0,0] cbsz:4 blgp:2
	v_mfma_scale_f32_16x16x128_f8f6f4 v[50:53], v[222:225], v[8:13], v[50:53], v177, v241 op_sel:[0,1,0] op_sel_hi:[0,0,0] cbsz:4 blgp:2
	v_mfma_scale_f32_16x16x128_f8f6f4 v[34:37], v[226:229], v[8:13], v[34:37], v177, v241 op_sel:[0,1,0] op_sel_hi:[0,0,0] cbsz:4 blgp:2
	v_mfma_scale_f32_16x16x128_f8f6f4 v[106:109], v[202:205], v[14:19], v[106:109], v177, v242 op_sel:[0,1,0] op_sel_hi:[0,0,0] cbsz:4 blgp:2
	v_mfma_scale_f32_16x16x128_f8f6f4 v[94:97], v[206:209], v[14:19], v[94:97], v177, v242 op_sel:[0,1,0] op_sel_hi:[0,0,0] cbsz:4 blgp:2
	v_mfma_scale_f32_16x16x128_f8f6f4 v[78:81], v[210:213], v[14:19], v[78:81], v177, v242 op_sel:[0,1,0] op_sel_hi:[0,0,0] cbsz:4 blgp:2
	v_mfma_scale_f32_16x16x128_f8f6f4 v[62:65], v[214:217], v[14:19], v[62:65], v177, v242 op_sel:[0,1,0] op_sel_hi:[0,0,0] cbsz:4 blgp:2
	v_mfma_scale_f32_16x16x128_f8f6f4 v[46:49], v[218:221], v[14:19], v[46:49], v177, v242 op_sel:[0,1,0] op_sel_hi:[0,0,0] cbsz:4 blgp:2
	v_mfma_scale_f32_16x16x128_f8f6f4 v[30:33], v[222:225], v[14:19], v[30:33], v177, v242 op_sel:[0,1,0] op_sel_hi:[0,0,0] cbsz:4 blgp:2
	v_mfma_scale_f32_16x16x128_f8f6f4 v[90:93], v[202:205], v[20:25], v[90:93], v177, v243 op_sel:[0,1,0] op_sel_hi:[0,0,0] cbsz:4 blgp:2
	v_mfma_scale_f32_16x16x128_f8f6f4 v[74:77], v[206:209], v[20:25], v[74:77], v177, v243 op_sel:[0,1,0] op_sel_hi:[0,0,0] cbsz:4 blgp:2
	v_mfma_scale_f32_16x16x128_f8f6f4 v[58:61], v[210:213], v[20:25], v[58:61], v177, v243 op_sel:[0,1,0] op_sel_hi:[0,0,0] cbsz:4 blgp:2
	v_mfma_scale_f32_16x16x128_f8f6f4 v[42:45], v[214:217], v[20:25], v[42:45], v177, v243 op_sel:[0,1,0] op_sel_hi:[0,0,0] cbsz:4 blgp:2
	v_mfma_scale_f32_16x16x128_f8f6f4 v[26:29], v[218:221], v[20:25], v[26:29], v177, v243 op_sel:[0,1,0] op_sel_hi:[0,0,0] cbsz:4 blgp:2
	v_mfma_scale_f32_16x16x128_f8f6f4 v[178:181], v[230:233], v[8:13], v[178:181], v177, v241 op_sel:[0,1,0] op_sel_hi:[0,0,0] cbsz:4 blgp:2
	v_mfma_scale_f32_16x16x128_f8f6f4 v[182:185], v[226:229], v[14:19], v[182:185], v177, v242 op_sel:[0,1,0] op_sel_hi:[0,0,0] cbsz:4 blgp:2
	v_mfma_scale_f32_16x16x128_f8f6f4 v[186:189], v[230:233], v[14:19], v[186:189], v177, v242 op_sel:[0,1,0] op_sel_hi:[0,0,0] cbsz:4 blgp:2
	v_mfma_scale_f32_16x16x128_f8f6f4 v[190:193], v[222:225], v[20:25], v[190:193], v177, v243 op_sel:[0,1,0] op_sel_hi:[0,0,0] cbsz:4 blgp:2
	v_mfma_scale_f32_16x16x128_f8f6f4 v[198:201], v[226:229], v[20:25], v[234:237], v177, v243 op_sel:[0,1,0] op_sel_hi:[0,0,0] cbsz:4 blgp:2
	v_mfma_scale_f32_16x16x128_f8f6f4 v[194:197], v[230:233], v[20:25], v[194:197], v177, v243 op_sel:[0,1,0] op_sel_hi:[0,0,0] cbsz:4 blgp:2
	s_barrier
	ds_read_b128 v[202:205], v166
	ds_read_b128 v[206:209], v166 offset:256
	ds_read_b128 v[210:213], v166 offset:512
	ds_read_b128 v[214:217], v166 offset:768
	ds_read_b128 v[218:221], v166 offset:1024
	ds_read_b128 v[222:225], v166 offset:1280
	ds_read_b128 v[226:229], v166 offset:1536
	ds_read_b128 v[230:233], v166 offset:1792
	ds_read2_b64 v[2:5], v162 offset1:1
	ds_read2_b64 v[6:9], v162 offset0:2 offset1:48
	ds_read2_b64 v[10:13], v162 offset0:49 offset1:50
	s_mov_b32 m0, s45
	ds_read2_b64 v[14:17], v162 offset0:96 offset1:97
	global_load_lds_dwordx4 v144, s[78:79]
	s_mov_b32 m0, s46
	ds_read2_b64 v[18:21], v162 offset0:98 offset1:144
	global_load_lds_dwordx4 v145, s[78:79]
	s_mov_b32 m0, s47
	ds_read2_b64 v[22:25], v162 offset0:145 offset1:146
	global_load_lds_dwordx4 v146, s[78:79]
	v_add_u32_e32 v234, s42, v176
	ds_read_u16 v242, v234
	ds_read_u16 v243, v234 offset:32
	ds_read_u16 v244, v234 offset:64
	s_and_b32 s42, s60, 0x1000
	s_add_i32 m0, s48, s42
	ds_read_u16 v245, v234 offset:96
	global_load_lds_dword v151, s[80:81]
	s_waitcnt vmcnt(6)
	s_waitcnt lgkmcnt(0)
	s_barrier
	v_mfma_scale_f32_16x16x128_f8f6f4 v[126:129], v[202:205], v[2:7], v[126:129], v177, v242 op_sel_hi:[0,0,0] cbsz:4 blgp:2
	v_mfma_scale_f32_16x16x128_f8f6f4 v[122:125], v[206:209], v[2:7], v[122:125], v177, v242 op_sel_hi:[0,0,0] cbsz:4 blgp:2
	v_mfma_scale_f32_16x16x128_f8f6f4 v[114:117], v[210:213], v[2:7], v[114:117], v177, v242 op_sel_hi:[0,0,0] cbsz:4 blgp:2
	v_mfma_scale_f32_16x16x128_f8f6f4 v[102:105], v[214:217], v[2:7], v[102:105], v177, v242 op_sel_hi:[0,0,0] cbsz:4 blgp:2
	v_mfma_scale_f32_16x16x128_f8f6f4 v[86:89], v[218:221], v[2:7], v[86:89], v177, v242 op_sel_hi:[0,0,0] cbsz:4 blgp:2
	v_mfma_scale_f32_16x16x128_f8f6f4 v[70:73], v[222:225], v[2:7], v[70:73], v177, v242 op_sel_hi:[0,0,0] cbsz:4 blgp:2
	v_mfma_scale_f32_16x16x128_f8f6f4 v[54:57], v[226:229], v[2:7], v[54:57], v177, v242 op_sel_hi:[0,0,0] cbsz:4 blgp:2
	v_mfma_scale_f32_16x16x128_f8f6f4 v[38:41], v[230:233], v[2:7], v[38:41], v177, v242 op_sel_hi:[0,0,0] cbsz:4 blgp:2
	v_mfma_scale_f32_16x16x128_f8f6f4 v[118:121], v[202:205], v[8:13], v[118:121], v177, v243 op_sel_hi:[0,0,0] cbsz:4 blgp:2
	v_mfma_scale_f32_16x16x128_f8f6f4 v[110:113], v[206:209], v[8:13], v[110:113], v177, v243 op_sel_hi:[0,0,0] cbsz:4 blgp:2
	v_mfma_scale_f32_16x16x128_f8f6f4 v[98:101], v[210:213], v[8:13], v[98:101], v177, v243 op_sel_hi:[0,0,0] cbsz:4 blgp:2
	v_mfma_scale_f32_16x16x128_f8f6f4 v[82:85], v[214:217], v[8:13], v[82:85], v177, v243 op_sel_hi:[0,0,0] cbsz:4 blgp:2
	v_mfma_scale_f32_16x16x128_f8f6f4 v[66:69], v[218:221], v[8:13], v[66:69], v177, v243 op_sel_hi:[0,0,0] cbsz:4 blgp:2
	v_mfma_scale_f32_16x16x128_f8f6f4 v[50:53], v[222:225], v[8:13], v[50:53], v177, v243 op_sel_hi:[0,0,0] cbsz:4 blgp:2
	v_mfma_scale_f32_16x16x128_f8f6f4 v[34:37], v[226:229], v[8:13], v[34:37], v177, v243 op_sel_hi:[0,0,0] cbsz:4 blgp:2
	v_mfma_scale_f32_16x16x128_f8f6f4 v[106:109], v[202:205], v[14:19], v[106:109], v177, v244 op_sel_hi:[0,0,0] cbsz:4 blgp:2
	v_mfma_scale_f32_16x16x128_f8f6f4 v[94:97], v[206:209], v[14:19], v[94:97], v177, v244 op_sel_hi:[0,0,0] cbsz:4 blgp:2
	v_mfma_scale_f32_16x16x128_f8f6f4 v[78:81], v[210:213], v[14:19], v[78:81], v177, v244 op_sel_hi:[0,0,0] cbsz:4 blgp:2
	v_mfma_scale_f32_16x16x128_f8f6f4 v[62:65], v[214:217], v[14:19], v[62:65], v177, v244 op_sel_hi:[0,0,0] cbsz:4 blgp:2
	v_mfma_scale_f32_16x16x128_f8f6f4 v[46:49], v[218:221], v[14:19], v[46:49], v177, v244 op_sel_hi:[0,0,0] cbsz:4 blgp:2
	v_mfma_scale_f32_16x16x128_f8f6f4 v[30:33], v[222:225], v[14:19], v[30:33], v177, v244 op_sel_hi:[0,0,0] cbsz:4 blgp:2
	v_mfma_scale_f32_16x16x128_f8f6f4 v[238:241], v[226:229], v[14:19], v[182:185], v177, v244 op_sel_hi:[0,0,0] cbsz:4 blgp:2
	v_mfma_scale_f32_16x16x128_f8f6f4 v[14:17], v[230:233], v[14:19], v[186:189], v177, v244 op_sel_hi:[0,0,0] cbsz:4 blgp:2
	v_mfma_scale_f32_16x16x128_f8f6f4 v[90:93], v[202:205], v[20:25], v[90:93], v177, v245 op_sel_hi:[0,0,0] cbsz:4 blgp:2
	v_mfma_scale_f32_16x16x128_f8f6f4 v[74:77], v[206:209], v[20:25], v[74:77], v177, v245 op_sel_hi:[0,0,0] cbsz:4 blgp:2
	v_mfma_scale_f32_16x16x128_f8f6f4 v[58:61], v[210:213], v[20:25], v[58:61], v177, v245 op_sel_hi:[0,0,0] cbsz:4 blgp:2
	v_mfma_scale_f32_16x16x128_f8f6f4 v[42:45], v[214:217], v[20:25], v[42:45], v177, v245 op_sel_hi:[0,0,0] cbsz:4 blgp:2
	v_mfma_scale_f32_16x16x128_f8f6f4 v[26:29], v[218:221], v[20:25], v[26:29], v177, v245 op_sel_hi:[0,0,0] cbsz:4 blgp:2
	v_mfma_scale_f32_16x16x128_f8f6f4 v[234:237], v[230:233], v[8:13], v[178:181], v177, v243 op_sel_hi:[0,0,0] cbsz:4 blgp:2
	v_mfma_scale_f32_16x16x128_f8f6f4 v[190:193], v[222:225], v[20:25], v[190:193], v177, v245 op_sel_hi:[0,0,0] cbsz:4 blgp:2
	v_mfma_scale_f32_16x16x128_f8f6f4 v[198:201], v[226:229], v[20:25], v[198:201], v177, v245 op_sel_hi:[0,0,0] cbsz:4 blgp:2
	v_mfma_scale_f32_16x16x128_f8f6f4 v[194:197], v[230:233], v[20:25], v[194:197], v177, v245 op_sel_hi:[0,0,0] cbsz:4 blgp:2
	s_barrier
	ds_read2_b64 v[2:5], v1 offset1:1
	s_mov_b32 m0, s51
	ds_read2_b64 v[6:9], v1 offset0:2 offset1:48
	global_load_lds_dwordx4 v147, s[78:79]
	s_mov_b32 m0, s53
	ds_read2_b64 v[10:13], v1 offset0:49 offset1:50
	global_load_lds_dwordx4 v148, s[78:79]
	s_mov_b32 m0, s54
	ds_read2_b64 v[178:181], v159 offset1:1
	global_load_lds_dwordx4 v149, s[78:79]
	s_mov_b32 m0, s61
	ds_read2_b64 v[182:185], v159 offset0:2 offset1:48
	global_load_lds_dwordx4 v142, s[74:75]
	s_mov_b32 m0, s58
	ds_read2_b64 v[186:189], v159 offset0:49 offset1:50
	global_load_lds_dwordx4 v143, s[74:75]
	s_waitcnt vmcnt(5)
	s_waitcnt lgkmcnt(0)
	s_barrier
	v_mfma_scale_f32_16x16x128_f8f6f4 v[126:129], v[202:205], v[2:7], v[126:129], v177, v242 op_sel:[0,1,0] op_sel_hi:[0,0,0] cbsz:4 blgp:2
	v_mfma_scale_f32_16x16x128_f8f6f4 v[122:125], v[206:209], v[2:7], v[122:125], v177, v242 op_sel:[0,1,0] op_sel_hi:[0,0,0] cbsz:4 blgp:2
	v_mfma_scale_f32_16x16x128_f8f6f4 v[114:117], v[210:213], v[2:7], v[114:117], v177, v242 op_sel:[0,1,0] op_sel_hi:[0,0,0] cbsz:4 blgp:2
	v_mfma_scale_f32_16x16x128_f8f6f4 v[102:105], v[214:217], v[2:7], v[102:105], v177, v242 op_sel:[0,1,0] op_sel_hi:[0,0,0] cbsz:4 blgp:2
	v_mfma_scale_f32_16x16x128_f8f6f4 v[86:89], v[218:221], v[2:7], v[86:89], v177, v242 op_sel:[0,1,0] op_sel_hi:[0,0,0] cbsz:4 blgp:2
	v_mfma_scale_f32_16x16x128_f8f6f4 v[70:73], v[222:225], v[2:7], v[70:73], v177, v242 op_sel:[0,1,0] op_sel_hi:[0,0,0] cbsz:4 blgp:2
	v_mfma_scale_f32_16x16x128_f8f6f4 v[54:57], v[226:229], v[2:7], v[54:57], v177, v242 op_sel:[0,1,0] op_sel_hi:[0,0,0] cbsz:4 blgp:2
	v_mfma_scale_f32_16x16x128_f8f6f4 v[38:41], v[230:233], v[2:7], v[38:41], v177, v242 op_sel:[0,1,0] op_sel_hi:[0,0,0] cbsz:4 blgp:2
	v_mfma_scale_f32_16x16x128_f8f6f4 v[118:121], v[202:205], v[8:13], v[118:121], v177, v243 op_sel:[0,1,0] op_sel_hi:[0,0,0] cbsz:4 blgp:2
	v_mfma_scale_f32_16x16x128_f8f6f4 v[110:113], v[206:209], v[8:13], v[110:113], v177, v243 op_sel:[0,1,0] op_sel_hi:[0,0,0] cbsz:4 blgp:2
	v_mfma_scale_f32_16x16x128_f8f6f4 v[98:101], v[210:213], v[8:13], v[98:101], v177, v243 op_sel:[0,1,0] op_sel_hi:[0,0,0] cbsz:4 blgp:2
	v_mfma_scale_f32_16x16x128_f8f6f4 v[82:85], v[214:217], v[8:13], v[82:85], v177, v243 op_sel:[0,1,0] op_sel_hi:[0,0,0] cbsz:4 blgp:2
	v_mfma_scale_f32_16x16x128_f8f6f4 v[66:69], v[218:221], v[8:13], v[66:69], v177, v243 op_sel:[0,1,0] op_sel_hi:[0,0,0] cbsz:4 blgp:2
	v_mfma_scale_f32_16x16x128_f8f6f4 v[50:53], v[222:225], v[8:13], v[50:53], v177, v243 op_sel:[0,1,0] op_sel_hi:[0,0,0] cbsz:4 blgp:2
	v_mfma_scale_f32_16x16x128_f8f6f4 v[34:37], v[226:229], v[8:13], v[34:37], v177, v243 op_sel:[0,1,0] op_sel_hi:[0,0,0] cbsz:4 blgp:2
	v_mfma_scale_f32_16x16x128_f8f6f4 v[22:25], v[230:233], v[8:13], v[234:237], v177, v243 op_sel:[0,1,0] op_sel_hi:[0,0,0] cbsz:4 blgp:2
	v_mfma_scale_f32_16x16x128_f8f6f4 v[106:109], v[202:205], v[178:183], v[106:109], v177, v244 op_sel:[0,1,0] op_sel_hi:[0,0,0] cbsz:4 blgp:2
	v_mfma_scale_f32_16x16x128_f8f6f4 v[94:97], v[206:209], v[178:183], v[94:97], v177, v244 op_sel:[0,1,0] op_sel_hi:[0,0,0] cbsz:4 blgp:2
	v_mfma_scale_f32_16x16x128_f8f6f4 v[78:81], v[210:213], v[178:183], v[78:81], v177, v244 op_sel:[0,1,0] op_sel_hi:[0,0,0] cbsz:4 blgp:2
	v_mfma_scale_f32_16x16x128_f8f6f4 v[62:65], v[214:217], v[178:183], v[62:65], v177, v244 op_sel:[0,1,0] op_sel_hi:[0,0,0] cbsz:4 blgp:2
	v_mfma_scale_f32_16x16x128_f8f6f4 v[46:49], v[218:221], v[178:183], v[46:49], v177, v244 op_sel:[0,1,0] op_sel_hi:[0,0,0] cbsz:4 blgp:2
	v_mfma_scale_f32_16x16x128_f8f6f4 v[30:33], v[222:225], v[178:183], v[30:33], v177, v244 op_sel:[0,1,0] op_sel_hi:[0,0,0] cbsz:4 blgp:2
	v_mfma_scale_f32_16x16x128_f8f6f4 v[18:21], v[226:229], v[178:183], v[238:241], v177, v244 op_sel:[0,1,0] op_sel_hi:[0,0,0] cbsz:4 blgp:2
	v_mfma_scale_f32_16x16x128_f8f6f4 v[10:13], v[230:233], v[178:183], v[14:17], v177, v244 op_sel:[0,1,0] op_sel_hi:[0,0,0] cbsz:4 blgp:2
	v_mfma_scale_f32_16x16x128_f8f6f4 v[90:93], v[202:205], v[184:189], v[90:93], v177, v245 op_sel:[0,1,0] op_sel_hi:[0,0,0] cbsz:4 blgp:2
	v_mfma_scale_f32_16x16x128_f8f6f4 v[74:77], v[206:209], v[184:189], v[74:77], v177, v245 op_sel:[0,1,0] op_sel_hi:[0,0,0] cbsz:4 blgp:2
	v_mfma_scale_f32_16x16x128_f8f6f4 v[58:61], v[210:213], v[184:189], v[58:61], v177, v245 op_sel:[0,1,0] op_sel_hi:[0,0,0] cbsz:4 blgp:2
	v_mfma_scale_f32_16x16x128_f8f6f4 v[42:45], v[214:217], v[184:189], v[42:45], v177, v245 op_sel:[0,1,0] op_sel_hi:[0,0,0] cbsz:4 blgp:2
	v_mfma_scale_f32_16x16x128_f8f6f4 v[26:29], v[218:221], v[184:189], v[26:29], v177, v245 op_sel:[0,1,0] op_sel_hi:[0,0,0] cbsz:4 blgp:2
	v_mfma_scale_f32_16x16x128_f8f6f4 v[14:17], v[222:225], v[184:189], v[190:193], v177, v245 op_sel:[0,1,0] op_sel_hi:[0,0,0] cbsz:4 blgp:2
	v_mfma_scale_f32_16x16x128_f8f6f4 v[6:9], v[226:229], v[184:189], v[198:201], v177, v245 op_sel:[0,1,0] op_sel_hi:[0,0,0] cbsz:4 blgp:2
	v_mfma_scale_f32_16x16x128_f8f6f4 v[2:5], v[230:233], v[184:189], v[194:197], v177, v245 op_sel:[0,1,0] op_sel_hi:[0,0,0] cbsz:4 blgp:2
	s_add_i32 s59, s59, 2
	s_addk_i32 s60, 0x1000
	s_add_u32 s72, s72, 0x8000
	s_addc_u32 s73, s73, 0
	s_add_u32 s74, s74, 0x8000
	s_addc_u32 s75, s75, 0
	s_add_u32 s76, s76, 0x18000
	s_addc_u32 s77, s77, 0
	s_add_u32 s78, s78, 0x18000
	s_addc_u32 s79, s79, 0
	s_add_u32 s80, s80, 0x1000
	s_addc_u32 s81, s81, 0
	s_add_i32 s42, s60, 0xfffff000
	s_and_b32 s42, s42, 0x1000
	s_cmp_lt_u32 s59, 28
	s_barrier
	s_cbranch_scc1 .LBB3_3
	ds_read_b128 v[154:157], v175
	ds_read_b128 v[186:189], v175 offset:256
	ds_read_b128 v[190:193], v175 offset:512
	ds_read_b128 v[194:197], v175 offset:768
	ds_read_b128 v[198:201], v175 offset:1024
	ds_read_b128 v[202:205], v175 offset:1280
	ds_read_b128 v[206:209], v175 offset:1536
	ds_read_b128 v[210:213], v175 offset:1792
	ds_read_b64 v[142:143], v171
	ds_read_b64 v[144:145], v171 offset:8
	ds_read_b64 v[146:147], v171 offset:16
	ds_read_b64 v[148:149], v174
	ds_read_b64 v[150:151], v174 offset:8
	ds_read_b64 v[152:153], v174 offset:16
	ds_read_b64 v[174:175], v173
	ds_read_b64 v[176:177], v173 offset:8
	ds_read_b64 v[178:179], v173 offset:16
	ds_read_b64 v[180:181], v172
	ds_read_b64 v[182:183], v172 offset:8
	ds_read_b64 v[184:185], v172 offset:16
	v_add_u32_e32 v171, 0x21000, v248
	v_add_u32_e32 v172, 0x21020, v248
	v_add_u32_e32 v173, 0x21040, v248
	v_add_u32_e32 v214, 0x21060, v248
	s_mov_b64 s[0:1], 0x7c000
	s_mov_b32 m0, s61
	ds_read_u16 v171, v171
	ds_read_u16 v215, v172
	ds_read_u16 v216, v173
	ds_read_u16 v214, v214
	v_lshl_add_u64 v[172:173], v[138:139], 0, s[0:1]
	s_mov_b64 s[0:1], 0x7e000
	v_lshl_add_u64 v[138:139], v[138:139], 0, s[0:1]
	s_mov_b32 m0, s58
	s_mov_b64 s[0:1], 0x174000
	v_lshl_add_u64 v[138:139], v[140:141], 0, s[0:1]
	v_lshl_add_u64 v[140:141], v[138:139], 0, s[16:17]
	s_mov_b32 m0, s57
	v_lshl_add_u64 v[130:131], s[14:15], 0, v[130:131]
	global_load_lds_dwordx4 v[140:141], off
	v_lshl_add_u64 v[140:141], v[138:139], 0, s[18:19]
	s_mov_b32 m0, s56
	v_lshl_add_u64 v[138:139], v[138:139], 0, s[20:21]
	global_load_lds_dwordx4 v[140:141], off
	s_mov_b32 m0, s55
	s_mov_b64 s[0:1], 0xf800
	global_load_lds_dwordx4 v[138:139], off
	v_lshl_add_u64 v[130:131], v[130:131], 0, s[0:1]
	s_add_i32 m0, s9, 0x21800
	s_waitcnt lgkmcnt(0)
	v_mov_b32_e32 v172, v216
	global_load_lds_dword v[130:131], off
	s_waitcnt vmcnt(6)
	s_waitcnt lgkmcnt(0)
	v_mov_b32_e32 v130, v171
	v_mov_b32_e32 v131, v215
	v_mov_b32_e32 v217, v214
	s_barrier
	v_mov_b32_e32 v161, 0x7f7f7f7f
	s_nop 1
	v_mfma_scale_f32_16x16x128_f8f6f4 v[126:129], v[154:157], v[142:147], v[126:129], v161, v130 op_sel_hi:[0,0,0] cbsz:4 blgp:2
	v_mfma_scale_f32_16x16x128_f8f6f4 v[122:125], v[186:189], v[142:147], v[122:125], v161, v130 op_sel_hi:[0,0,0] cbsz:4 blgp:2
	v_mfma_scale_f32_16x16x128_f8f6f4 v[114:117], v[190:193], v[142:147], v[114:117], v161, v130 op_sel_hi:[0,0,0] cbsz:4 blgp:2
	v_mfma_scale_f32_16x16x128_f8f6f4 v[102:105], v[194:197], v[142:147], v[102:105], v161, v130 op_sel_hi:[0,0,0] cbsz:4 blgp:2
	v_mfma_scale_f32_16x16x128_f8f6f4 v[86:89], v[198:201], v[142:147], v[86:89], v161, v130 op_sel_hi:[0,0,0] cbsz:4 blgp:2
	v_mfma_scale_f32_16x16x128_f8f6f4 v[70:73], v[202:205], v[142:147], v[70:73], v161, v130 op_sel_hi:[0,0,0] cbsz:4 blgp:2
	v_mfma_scale_f32_16x16x128_f8f6f4 v[54:57], v[206:209], v[142:147], v[54:57], v161, v130 op_sel_hi:[0,0,0] cbsz:4 blgp:2
	v_mfma_scale_f32_16x16x128_f8f6f4 v[38:41], v[210:213], v[142:147], v[38:41], v161, v130 op_sel_hi:[0,0,0] cbsz:4 blgp:2
	v_mfma_scale_f32_16x16x128_f8f6f4 v[118:121], v[154:157], v[148:153], v[118:121], v161, v131 op_sel_hi:[0,0,0] cbsz:4 blgp:2
	v_mfma_scale_f32_16x16x128_f8f6f4 v[110:113], v[186:189], v[148:153], v[110:113], v161, v131 op_sel_hi:[0,0,0] cbsz:4 blgp:2
	v_mfma_scale_f32_16x16x128_f8f6f4 v[98:101], v[190:193], v[148:153], v[98:101], v161, v131 op_sel_hi:[0,0,0] cbsz:4 blgp:2
	v_mfma_scale_f32_16x16x128_f8f6f4 v[82:85], v[194:197], v[148:153], v[82:85], v161, v131 op_sel_hi:[0,0,0] cbsz:4 blgp:2
	v_mfma_scale_f32_16x16x128_f8f6f4 v[66:69], v[198:201], v[148:153], v[66:69], v161, v131 op_sel_hi:[0,0,0] cbsz:4 blgp:2
	v_mfma_scale_f32_16x16x128_f8f6f4 v[50:53], v[202:205], v[148:153], v[50:53], v161, v131 op_sel_hi:[0,0,0] cbsz:4 blgp:2
	v_mfma_scale_f32_16x16x128_f8f6f4 v[34:37], v[206:209], v[148:153], v[34:37], v161, v131 op_sel_hi:[0,0,0] cbsz:4 blgp:2
	v_mfma_scale_f32_16x16x128_f8f6f4 v[138:141], v[210:213], v[148:153], v[22:25], v161, v131 op_sel_hi:[0,0,0] cbsz:4 blgp:2
	v_mfma_scale_f32_16x16x128_f8f6f4 v[106:109], v[154:157], v[174:179], v[106:109], v161, v172 op_sel_hi:[0,0,0] cbsz:4 blgp:2
	v_mfma_scale_f32_16x16x128_f8f6f4 v[94:97], v[186:189], v[174:179], v[94:97], v161, v172 op_sel_hi:[0,0,0] cbsz:4 blgp:2
	v_mfma_scale_f32_16x16x128_f8f6f4 v[78:81], v[190:193], v[174:179], v[78:81], v161, v172 op_sel_hi:[0,0,0] cbsz:4 blgp:2
	v_mfma_scale_f32_16x16x128_f8f6f4 v[62:65], v[194:197], v[174:179], v[62:65], v161, v172 op_sel_hi:[0,0,0] cbsz:4 blgp:2
	v_mfma_scale_f32_16x16x128_f8f6f4 v[46:49], v[198:201], v[174:179], v[46:49], v161, v172 op_sel_hi:[0,0,0] cbsz:4 blgp:2
	v_mfma_scale_f32_16x16x128_f8f6f4 v[142:145], v[206:209], v[174:179], v[18:21], v161, v172 op_sel_hi:[0,0,0] cbsz:4 blgp:2
	v_mfma_scale_f32_16x16x128_f8f6f4 v[146:149], v[210:213], v[174:179], v[10:13], v161, v172 op_sel_hi:[0,0,0] cbsz:4 blgp:2
	v_mfma_scale_f32_16x16x128_f8f6f4 v[90:93], v[154:157], v[180:185], v[90:93], v161, v217 op_sel_hi:[0,0,0] cbsz:4 blgp:2
	v_mfma_scale_f32_16x16x128_f8f6f4 v[74:77], v[186:189], v[180:185], v[74:77], v161, v217 op_sel_hi:[0,0,0] cbsz:4 blgp:2
	v_mfma_scale_f32_16x16x128_f8f6f4 v[58:61], v[190:193], v[180:185], v[58:61], v161, v217 op_sel_hi:[0,0,0] cbsz:4 blgp:2
	v_mfma_scale_f32_16x16x128_f8f6f4 v[150:153], v[202:205], v[180:185], v[14:17], v161, v217 op_sel_hi:[0,0,0] cbsz:4 blgp:2
	v_mfma_scale_f32_16x16x128_f8f6f4 v[30:33], v[202:205], v[174:179], v[30:33], v161, v172 op_sel_hi:[0,0,0] cbsz:4 blgp:2
	v_mfma_scale_f32_16x16x128_f8f6f4 v[42:45], v[194:197], v[180:185], v[42:45], v161, v217 op_sel_hi:[0,0,0] cbsz:4 blgp:2
	v_mfma_scale_f32_16x16x128_f8f6f4 v[26:29], v[198:201], v[180:185], v[26:29], v161, v217 op_sel_hi:[0,0,0] cbsz:4 blgp:2
	v_mfma_scale_f32_16x16x128_f8f6f4 v[172:175], v[206:209], v[180:185], v[6:9], v161, v217 op_sel_hi:[0,0,0] cbsz:4 blgp:2
	v_mfma_scale_f32_16x16x128_f8f6f4 v[176:179], v[210:213], v[180:185], v[2:5], v161, v217 op_sel_hi:[0,0,0] cbsz:4 blgp:2
	s_barrier
	ds_read_b64 v[2:3], v167
	ds_read_b64 v[4:5], v167 offset:8
	ds_read_b64 v[6:7], v167 offset:16
	ds_read_b64 v[8:9], v170
	ds_read_b64 v[10:11], v170 offset:8
	ds_read_b64 v[12:13], v170 offset:16
	ds_read_b64 v[14:15], v169
	ds_read_b64 v[16:17], v169 offset:8
	ds_read_b64 v[18:19], v169 offset:16
	s_mov_b64 s[0:1], 0x175800
	s_mov_b32 m0, s52
	ds_read_b64 v[20:21], v168
	ds_read_b64 v[22:23], v168 offset:8
	ds_read_b64 v[24:25], v168 offset:16
	v_lshl_add_u64 v[130:131], v[132:133], 0, s[0:1]
	global_load_lds_dwordx4 v[130:131], off
	v_lshl_add_u64 v[130:131], v[134:135], 0, s[0:1]
	s_mov_b32 m0, s50
	v_lshrrev_b32_e32 v167, 8, v216
	global_load_lds_dwordx4 v[130:131], off
	v_lshl_add_u64 v[130:131], v[136:137], 0, s[0:1]
	s_mov_b32 m0, s49
	v_lshrrev_b32_e32 v168, 8, v214
	global_load_lds_dwordx4 v[130:131], off
	s_waitcnt vmcnt(3)
	s_waitcnt lgkmcnt(0)
	v_lshrrev_b32_e32 v130, 8, v171
	v_lshrrev_b32_e32 v131, 8, v215
	s_barrier
	v_mfma_scale_f32_16x16x128_f8f6f4 v[126:129], v[154:157], v[2:7], v[126:129], v161, v130 op_sel_hi:[0,0,0] cbsz:4 blgp:2
	v_mfma_scale_f32_16x16x128_f8f6f4 v[122:125], v[186:189], v[2:7], v[122:125], v161, v130 op_sel_hi:[0,0,0] cbsz:4 blgp:2
	v_mfma_scale_f32_16x16x128_f8f6f4 v[114:117], v[190:193], v[2:7], v[114:117], v161, v130 op_sel_hi:[0,0,0] cbsz:4 blgp:2
	v_mfma_scale_f32_16x16x128_f8f6f4 v[102:105], v[194:197], v[2:7], v[102:105], v161, v130 op_sel_hi:[0,0,0] cbsz:4 blgp:2
	v_mfma_scale_f32_16x16x128_f8f6f4 v[86:89], v[198:201], v[2:7], v[86:89], v161, v130 op_sel_hi:[0,0,0] cbsz:4 blgp:2
	v_mfma_scale_f32_16x16x128_f8f6f4 v[70:73], v[202:205], v[2:7], v[70:73], v161, v130 op_sel_hi:[0,0,0] cbsz:4 blgp:2
	v_mfma_scale_f32_16x16x128_f8f6f4 v[54:57], v[206:209], v[2:7], v[54:57], v161, v130 op_sel_hi:[0,0,0] cbsz:4 blgp:2
	v_mfma_scale_f32_16x16x128_f8f6f4 v[38:41], v[210:213], v[2:7], v[38:41], v161, v130 op_sel_hi:[0,0,0] cbsz:4 blgp:2
	v_mfma_scale_f32_16x16x128_f8f6f4 v[118:121], v[154:157], v[8:13], v[118:121], v161, v131 op_sel_hi:[0,0,0] cbsz:4 blgp:2
	v_mfma_scale_f32_16x16x128_f8f6f4 v[110:113], v[186:189], v[8:13], v[110:113], v161, v131 op_sel_hi:[0,0,0] cbsz:4 blgp:2
	v_mfma_scale_f32_16x16x128_f8f6f4 v[98:101], v[190:193], v[8:13], v[98:101], v161, v131 op_sel_hi:[0,0,0] cbsz:4 blgp:2
	v_mfma_scale_f32_16x16x128_f8f6f4 v[82:85], v[194:197], v[8:13], v[82:85], v161, v131 op_sel_hi:[0,0,0] cbsz:4 blgp:2
	v_mfma_scale_f32_16x16x128_f8f6f4 v[66:69], v[198:201], v[8:13], v[66:69], v161, v131 op_sel_hi:[0,0,0] cbsz:4 blgp:2
	v_mfma_scale_f32_16x16x128_f8f6f4 v[50:53], v[202:205], v[8:13], v[50:53], v161, v131 op_sel_hi:[0,0,0] cbsz:4 blgp:2
	v_mfma_scale_f32_16x16x128_f8f6f4 v[34:37], v[206:209], v[8:13], v[34:37], v161, v131 op_sel_hi:[0,0,0] cbsz:4 blgp:2
	v_mfma_scale_f32_16x16x128_f8f6f4 v[130:133], v[210:213], v[8:13], v[138:141], v161, v131 op_sel_hi:[0,0,0] cbsz:4 blgp:2
	v_mfma_scale_f32_16x16x128_f8f6f4 v[106:109], v[154:157], v[14:19], v[106:109], v161, v167 op_sel_hi:[0,0,0] cbsz:4 blgp:2
	v_mfma_scale_f32_16x16x128_f8f6f4 v[94:97], v[186:189], v[14:19], v[94:97], v161, v167 op_sel_hi:[0,0,0] cbsz:4 blgp:2
	v_mfma_scale_f32_16x16x128_f8f6f4 v[78:81], v[190:193], v[14:19], v[78:81], v161, v167 op_sel_hi:[0,0,0] cbsz:4 blgp:2
	v_mfma_scale_f32_16x16x128_f8f6f4 v[62:65], v[194:197], v[14:19], v[62:65], v161, v167 op_sel_hi:[0,0,0] cbsz:4 blgp:2
	v_mfma_scale_f32_16x16x128_f8f6f4 v[46:49], v[198:201], v[14:19], v[46:49], v161, v167 op_sel_hi:[0,0,0] cbsz:4 blgp:2
	v_mfma_scale_f32_16x16x128_f8f6f4 v[134:137], v[206:209], v[14:19], v[142:145], v161, v167 op_sel_hi:[0,0,0] cbsz:4 blgp:2
	v_mfma_scale_f32_16x16x128_f8f6f4 v[138:141], v[210:213], v[14:19], v[146:149], v161, v167 op_sel_hi:[0,0,0] cbsz:4 blgp:2
	v_mfma_scale_f32_16x16x128_f8f6f4 v[90:93], v[154:157], v[20:25], v[90:93], v161, v168 op_sel_hi:[0,0,0] cbsz:4 blgp:2
	v_mfma_scale_f32_16x16x128_f8f6f4 v[58:61], v[190:193], v[20:25], v[58:61], v161, v168 op_sel_hi:[0,0,0] cbsz:4 blgp:2
	v_mfma_scale_f32_16x16x128_f8f6f4 v[142:145], v[202:205], v[20:25], v[150:153], v161, v168 op_sel_hi:[0,0,0] cbsz:4 blgp:2
	v_mfma_scale_f32_16x16x128_f8f6f4 v[146:149], v[206:209], v[20:25], v[172:175], v161, v168 op_sel_hi:[0,0,0] cbsz:4 blgp:2
	v_mfma_scale_f32_16x16x128_f8f6f4 v[150:153], v[210:213], v[20:25], v[176:179], v161, v168 op_sel_hi:[0,0,0] cbsz:4 blgp:2
	v_mfma_scale_f32_16x16x128_f8f6f4 v[30:33], v[202:205], v[14:19], v[30:33], v161, v167 op_sel_hi:[0,0,0] cbsz:4 blgp:2
	v_mfma_scale_f32_16x16x128_f8f6f4 v[236:239], v[186:189], v[20:25], v[74:77], v161, v168 op_sel_hi:[0,0,0] cbsz:4 blgp:2
	v_mfma_scale_f32_16x16x128_f8f6f4 v[42:45], v[194:197], v[20:25], v[42:45], v161, v168 op_sel_hi:[0,0,0] cbsz:4 blgp:2
	v_mfma_scale_f32_16x16x128_f8f6f4 v[26:29], v[198:201], v[20:25], v[26:29], v161, v168 op_sel_hi:[0,0,0] cbsz:4 blgp:2
	s_barrier
	ds_read_b128 v[168:171], v166
	ds_read_b128 v[172:175], v166 offset:256
	ds_read_b128 v[176:179], v166 offset:512
	ds_read_b128 v[180:183], v166 offset:768
	ds_read_b128 v[184:187], v166 offset:1024
	ds_read_b128 v[188:191], v166 offset:1280
	ds_read_b128 v[192:195], v166 offset:1536
	ds_read_b128 v[196:199], v166 offset:1792
	ds_read_b64 v[2:3], v162
	ds_read_b64 v[4:5], v162 offset:8
	ds_read_b64 v[6:7], v162 offset:16
	ds_read_b64 v[8:9], v165
	ds_read_b64 v[10:11], v165 offset:8
	ds_read_b64 v[12:13], v165 offset:16
	ds_read_b64 v[14:15], v164
	ds_read_b64 v[16:17], v164 offset:8
	ds_read_b64 v[18:19], v164 offset:16
	ds_read_b64 v[20:21], v163
	ds_read_b64 v[22:23], v163 offset:8
	ds_read_b64 v[24:25], v163 offset:16
	v_add_u32_e32 v154, 0x21800, v248
	v_add_u32_e32 v155, 0x21820, v248
	v_add_u32_e32 v156, 0x21840, v248
	v_add_u32_e32 v157, 0x21860, v248
	ds_read_u16 v166, v154
	ds_read_u16 v167, v155
	ds_read_u16 v74, v156
	ds_read_u16 v75, v157
	s_waitcnt vmcnt(0)
	s_waitcnt lgkmcnt(0)
	s_waitcnt lgkmcnt(0)
	v_mov_b32_e32 v76, v166
	v_mov_b32_e32 v77, v167
	v_mov_b32_e32 v228, v74
	v_mov_b32_e32 v252, v75
	s_barrier
	v_mfma_scale_f32_16x16x128_f8f6f4 v[126:129], v[168:171], v[2:7], v[126:129], v161, v76 op_sel_hi:[0,0,0] cbsz:4 blgp:2
	v_mfma_scale_f32_16x16x128_f8f6f4 v[122:125], v[172:175], v[2:7], v[122:125], v161, v76 op_sel_hi:[0,0,0] cbsz:4 blgp:2
	v_mfma_scale_f32_16x16x128_f8f6f4 v[114:117], v[176:179], v[2:7], v[114:117], v161, v76 op_sel_hi:[0,0,0] cbsz:4 blgp:2
	v_mfma_scale_f32_16x16x128_f8f6f4 v[102:105], v[180:183], v[2:7], v[102:105], v161, v76 op_sel_hi:[0,0,0] cbsz:4 blgp:2
	v_mfma_scale_f32_16x16x128_f8f6f4 v[86:89], v[184:187], v[2:7], v[86:89], v161, v76 op_sel_hi:[0,0,0] cbsz:4 blgp:2
	v_mfma_scale_f32_16x16x128_f8f6f4 v[70:73], v[188:191], v[2:7], v[70:73], v161, v76 op_sel_hi:[0,0,0] cbsz:4 blgp:2
	v_mfma_scale_f32_16x16x128_f8f6f4 v[54:57], v[192:195], v[2:7], v[54:57], v161, v76 op_sel_hi:[0,0,0] cbsz:4 blgp:2
	v_mfma_scale_f32_16x16x128_f8f6f4 v[154:157], v[196:199], v[2:7], v[38:41], v161, v76 op_sel_hi:[0,0,0] cbsz:4 blgp:2
	v_mfma_scale_f32_16x16x128_f8f6f4 v[118:121], v[168:171], v[8:13], v[118:121], v161, v77 op_sel_hi:[0,0,0] cbsz:4 blgp:2
	v_mfma_scale_f32_16x16x128_f8f6f4 v[82:85], v[180:183], v[8:13], v[82:85], v161, v77 op_sel_hi:[0,0,0] cbsz:4 blgp:2
	v_mfma_scale_f32_16x16x128_f8f6f4 v[66:69], v[184:187], v[8:13], v[66:69], v161, v77 op_sel_hi:[0,0,0] cbsz:4 blgp:2
	v_mfma_scale_f32_16x16x128_f8f6f4 v[50:53], v[188:191], v[8:13], v[50:53], v161, v77 op_sel_hi:[0,0,0] cbsz:4 blgp:2
	v_mfma_scale_f32_16x16x128_f8f6f4 v[130:133], v[196:199], v[8:13], v[130:133], v161, v77 op_sel_hi:[0,0,0] cbsz:4 blgp:2
	v_mfma_scale_f32_16x16x128_f8f6f4 v[62:65], v[180:183], v[14:19], v[62:65], v161, v228 op_sel_hi:[0,0,0] cbsz:4 blgp:2
	v_mfma_scale_f32_16x16x128_f8f6f4 v[46:49], v[184:187], v[14:19], v[46:49], v161, v228 op_sel_hi:[0,0,0] cbsz:4 blgp:2
	v_mfma_scale_f32_16x16x128_f8f6f4 v[58:61], v[176:179], v[20:25], v[58:61], v161, v252 op_sel_hi:[0,0,0] cbsz:4 blgp:2
	v_mfma_scale_f32_16x16x128_f8f6f4 v[162:165], v[172:175], v[8:13], v[110:113], v161, v77 op_sel_hi:[0,0,0] cbsz:4 blgp:2
	v_mfma_scale_f32_16x16x128_f8f6f4 v[200:203], v[176:179], v[8:13], v[98:101], v161, v77 op_sel_hi:[0,0,0] cbsz:4 blgp:2
	v_mfma_scale_f32_16x16x128_f8f6f4 v[204:207], v[192:195], v[8:13], v[34:37], v161, v77 op_sel_hi:[0,0,0] cbsz:4 blgp:2
	v_mfma_scale_f32_16x16x128_f8f6f4 v[208:211], v[168:171], v[14:19], v[106:109], v161, v228 op_sel_hi:[0,0,0] cbsz:4 blgp:2
	v_mfma_scale_f32_16x16x128_f8f6f4 v[212:215], v[172:175], v[14:19], v[94:97], v161, v228 op_sel_hi:[0,0,0] cbsz:4 blgp:2
	v_mfma_scale_f32_16x16x128_f8f6f4 v[216:219], v[176:179], v[14:19], v[78:81], v161, v228 op_sel_hi:[0,0,0] cbsz:4 blgp:2
	v_mfma_scale_f32_16x16x128_f8f6f4 v[220:223], v[188:191], v[14:19], v[30:33], v161, v228 op_sel_hi:[0,0,0] cbsz:4 blgp:2
	v_mfma_scale_f32_16x16x128_f8f6f4 v[224:227], v[192:195], v[14:19], v[134:137], v161, v228 op_sel_hi:[0,0,0] cbsz:4 blgp:2
	v_mfma_scale_f32_16x16x128_f8f6f4 v[228:231], v[196:199], v[14:19], v[138:141], v161, v228 op_sel_hi:[0,0,0] cbsz:4 blgp:2
	v_mfma_scale_f32_16x16x128_f8f6f4 v[232:235], v[168:171], v[20:25], v[90:93], v161, v252 op_sel_hi:[0,0,0] cbsz:4 blgp:2
	v_mfma_scale_f32_16x16x128_f8f6f4 v[236:239], v[172:175], v[20:25], v[236:239], v161, v252 op_sel_hi:[0,0,0] cbsz:4 blgp:2
	v_mfma_scale_f32_16x16x128_f8f6f4 v[42:45], v[180:183], v[20:25], v[42:45], v161, v252 op_sel_hi:[0,0,0] cbsz:4 blgp:2
	v_mfma_scale_f32_16x16x128_f8f6f4 v[240:243], v[184:187], v[20:25], v[26:29], v161, v252 op_sel_hi:[0,0,0] cbsz:4 blgp:2
	v_mfma_scale_f32_16x16x128_f8f6f4 v[244:247], v[188:191], v[20:25], v[142:145], v161, v252 op_sel_hi:[0,0,0] cbsz:4 blgp:2
	v_mfma_scale_f32_16x16x128_f8f6f4 v[248:251], v[192:195], v[20:25], v[146:149], v161, v252 op_sel_hi:[0,0,0] cbsz:4 blgp:2
	v_mfma_scale_f32_16x16x128_f8f6f4 v[252:255], v[196:199], v[20:25], v[150:153], v161, v252 op_sel_hi:[0,0,0] cbsz:4 blgp:2
	s_barrier
	ds_read_b64 v[18:19], v1
	ds_read_b64 v[20:21], v1 offset:8
	ds_read_b64 v[22:23], v1 offset:16
	ds_read_b64 v[24:25], v160
	ds_read_b64 v[26:27], v160 offset:8
	ds_read_b64 v[28:29], v160 offset:16
	ds_read_b64 v[30:31], v159
	ds_read_b64 v[32:33], v159 offset:8
	ds_read_b64 v[34:35], v159 offset:16
	ds_read_b64 v[36:37], v158
	ds_read_b64 v[38:39], v158 offset:8
	ds_read_b64 v[40:41], v158 offset:16
	s_waitcnt lgkmcnt(0)
	v_lshrrev_b32_e32 v1, 8, v166
	v_lshrrev_b32_e32 v76, 8, v167
	v_lshrrev_b32_e32 v112, 8, v74
	v_lshrrev_b32_e32 v160, 8, v75
	s_barrier
	v_mfma_scale_f32_16x16x128_f8f6f4 v[14:17], v[168:171], v[18:23], v[126:129], v161, v1 op_sel_hi:[0,0,0] cbsz:4 blgp:2
	v_mfma_scale_f32_16x16x128_f8f6f4 v[10:13], v[172:175], v[18:23], v[122:125], v161, v1 op_sel_hi:[0,0,0] cbsz:4 blgp:2
	v_mfma_scale_f32_16x16x128_f8f6f4 v[6:9], v[176:179], v[18:23], v[114:117], v161, v1 op_sel_hi:[0,0,0] cbsz:4 blgp:2
	v_mfma_scale_f32_16x16x128_f8f6f4 v[2:5], v[180:183], v[18:23], v[102:105], v161, v1 op_sel_hi:[0,0,0] cbsz:4 blgp:2
	v_mfma_scale_f32_16x16x128_f8f6f4 v[108:111], v[184:187], v[18:23], v[86:89], v161, v1 op_sel_hi:[0,0,0] cbsz:4 blgp:2
	v_mfma_scale_f32_16x16x128_f8f6f4 v[104:107], v[188:191], v[18:23], v[70:73], v161, v1 op_sel_hi:[0,0,0] cbsz:4 blgp:2
	v_mfma_scale_f32_16x16x128_f8f6f4 v[100:103], v[192:195], v[18:23], v[54:57], v161, v1 op_sel_hi:[0,0,0] cbsz:4 blgp:2
	v_mfma_scale_f32_16x16x128_f8f6f4 v[96:99], v[196:199], v[18:23], v[154:157], v161, v1 op_sel_hi:[0,0,0] cbsz:4 blgp:2
	v_mfma_scale_f32_16x16x128_f8f6f4 v[156:159], v[168:171], v[24:29], v[118:121], v161, v76 op_sel_hi:[0,0,0] cbsz:4 blgp:2
	v_mfma_scale_f32_16x16x128_f8f6f4 v[152:155], v[172:175], v[24:29], v[162:165], v161, v76 op_sel_hi:[0,0,0] cbsz:4 blgp:2
	v_mfma_scale_f32_16x16x128_f8f6f4 v[148:151], v[176:179], v[24:29], v[200:203], v161, v76 op_sel_hi:[0,0,0] cbsz:4 blgp:2
	v_mfma_scale_f32_16x16x128_f8f6f4 v[144:147], v[180:183], v[24:29], v[82:85], v161, v76 op_sel_hi:[0,0,0] cbsz:4 blgp:2
	v_mfma_scale_f32_16x16x128_f8f6f4 v[92:95], v[184:187], v[24:29], v[66:69], v161, v76 op_sel_hi:[0,0,0] cbsz:4 blgp:2
	v_mfma_scale_f32_16x16x128_f8f6f4 v[88:91], v[188:191], v[24:29], v[50:53], v161, v76 op_sel_hi:[0,0,0] cbsz:4 blgp:2
	v_mfma_scale_f32_16x16x128_f8f6f4 v[84:87], v[192:195], v[24:29], v[204:207], v161, v76 op_sel_hi:[0,0,0] cbsz:4 blgp:2
	v_mfma_scale_f32_16x16x128_f8f6f4 v[80:83], v[196:199], v[24:29], v[130:133], v161, v76 op_sel_hi:[0,0,0] cbsz:4 blgp:2
	v_mfma_scale_f32_16x16x128_f8f6f4 v[140:143], v[168:171], v[30:35], v[208:211], v161, v112 op_sel_hi:[0,0,0] cbsz:4 blgp:2
	v_mfma_scale_f32_16x16x128_f8f6f4 v[136:139], v[172:175], v[30:35], v[212:215], v161, v112 op_sel_hi:[0,0,0] cbsz:4 blgp:2
	v_mfma_scale_f32_16x16x128_f8f6f4 v[132:135], v[176:179], v[30:35], v[216:219], v161, v112 op_sel_hi:[0,0,0] cbsz:4 blgp:2
	v_mfma_scale_f32_16x16x128_f8f6f4 v[128:131], v[180:183], v[30:35], v[62:65], v161, v112 op_sel_hi:[0,0,0] cbsz:4 blgp:2
	v_mfma_scale_f32_16x16x128_f8f6f4 v[76:79], v[184:187], v[30:35], v[46:49], v161, v112 op_sel_hi:[0,0,0] cbsz:4 blgp:2
	v_mfma_scale_f32_16x16x128_f8f6f4 v[72:75], v[188:191], v[30:35], v[220:223], v161, v112 op_sel_hi:[0,0,0] cbsz:4 blgp:2
	v_mfma_scale_f32_16x16x128_f8f6f4 v[68:71], v[192:195], v[30:35], v[224:227], v161, v112 op_sel_hi:[0,0,0] cbsz:4 blgp:2
	v_mfma_scale_f32_16x16x128_f8f6f4 v[64:67], v[196:199], v[30:35], v[228:231], v161, v112 op_sel_hi:[0,0,0] cbsz:4 blgp:2
	v_mfma_scale_f32_16x16x128_f8f6f4 v[124:127], v[168:171], v[36:41], v[232:235], v161, v160 op_sel_hi:[0,0,0] cbsz:4 blgp:2
	v_mfma_scale_f32_16x16x128_f8f6f4 v[120:123], v[172:175], v[36:41], v[236:239], v161, v160 op_sel_hi:[0,0,0] cbsz:4 blgp:2
	v_mfma_scale_f32_16x16x128_f8f6f4 v[116:119], v[176:179], v[36:41], v[58:61], v161, v160 op_sel_hi:[0,0,0] cbsz:4 blgp:2
	v_mfma_scale_f32_16x16x128_f8f6f4 v[112:115], v[180:183], v[36:41], v[42:45], v161, v160 op_sel_hi:[0,0,0] cbsz:4 blgp:2
	v_mfma_scale_f32_16x16x128_f8f6f4 v[60:63], v[184:187], v[36:41], v[240:243], v161, v160 op_sel_hi:[0,0,0] cbsz:4 blgp:2
	v_mfma_scale_f32_16x16x128_f8f6f4 v[56:59], v[188:191], v[36:41], v[244:247], v161, v160 op_sel_hi:[0,0,0] cbsz:4 blgp:2
	v_mfma_scale_f32_16x16x128_f8f6f4 v[52:55], v[192:195], v[36:41], v[248:251], v161, v160 op_sel_hi:[0,0,0] cbsz:4 blgp:2
	v_mfma_scale_f32_16x16x128_f8f6f4 v[48:51], v[196:199], v[36:41], v[252:255], v161, v160 op_sel_hi:[0,0,0] cbsz:4 blgp:2
	s_barrier
	s_cmpk_gt_u32 s33, 0xff
	s_cbranch_scc1 .LBB3_6
	s_barrier
